# NSA tile loop: online-softmax accumulators kept in place (no per-tile register copies); P0 queue atomic wait deferred
# baseline (speedup 1.0000x reference)
.LBB0_66:
	s_and_saveexec_b64 s[0:1], s[4:5]
	s_cbranch_execz .LBB0_70
	v_mov_b32_e32 v200, 1
	global_atomic_add v200, v3, v200, s[10:11] sc0

.LBB0_264:
	s_lshl_b32 s14, s36, 2
	s_add_i32 s14, s14, 0
	s_add_i32 s14, s14, 0x23c80
	v_mov_b32_e32 v2, s14
	s_waitcnt vmcnt(4)
	ds_write_b32 v2, v200
	s_branch .LBB0_65

.LBB0_559:
	v_readlane_b32 s0, v249, 3
	v_mov_b32_e32 v3, v114
	s_add_i32 s0, s40, s0
	v_readlane_b32 s2, v250, 52
	v_permlane32_swap_b32_e32 v114, v3
	v_readlane_b32 s1, v249, 4
	v_readlane_b32 s3, v250, 53
	s_add_u32 s0, s0, s2
	v_add_f32_e32 v3, v114, v3
	s_addc_u32 s1, 0, s3
	v_div_scale_f32 v4, s[2:3], v3, v3, 1.0
	v_rcp_f32_e32 v5, v4
	s_lshl_b64 s[0:1], s[0:1], 11
	s_add_u32 s0, s60, s0
	s_addc_u32 s1, s61, s1
	v_fma_f32 v6, -v4, v5, 1.0
	v_fmac_f32_e32 v5, v6, v5
	v_div_scale_f32 v6, vcc, 1.0, v3, 1.0
	v_mul_f32_e32 v7, v6, v5
	v_fma_f32 v8, -v4, v7, v6
	v_fmac_f32_e32 v7, v8, v5
	v_fma_f32 v4, -v4, v7, v6
	v_div_fmas_f32 v4, v4, v5, v7
	v_readlane_b32 s2, v249, 5
	v_div_fixup_f32 v4, v4, v3, 1.0
	v_cmp_lt_f32_e32 vcc, 0, v3
	s_waitcnt vmcnt(0) lgkmcnt(0)
	s_barrier
	s_add_u32 s0, s0, s2
	v_readlane_b32 s93, v250, 10
	v_cndmask_b32_e32 v3, 0, v4, vcc
	s_addc_u32 s1, s1, 0
	v_mul_f32_e32 v4, v183, v3
	v_readlane_b32 s3, v249, 6
	v_pk_fma_f32 v[6:7], v[66:67], v[4:5], v[34:35] op_sel_hi:[1,0,1]
	v_pk_fma_f32 v[8:9], v[50:51], v[4:5], v[18:19] op_sel_hi:[1,0,1]
	v_pk_fma_f32 v[10:11], v[68:69], v[4:5], v[36:37] op_sel_hi:[1,0,1]
	v_pk_fma_f32 v[12:13], v[52:53], v[4:5], v[20:21] op_sel_hi:[1,0,1]
	v_pk_fma_f32 v[14:15], v[70:71], v[4:5], v[38:39] op_sel_hi:[1,0,1]
	v_pk_fma_f32 v[16:17], v[54:55], v[4:5], v[22:23] op_sel_hi:[1,0,1]
	v_pk_fma_f32 v[18:19], v[72:73], v[4:5], v[40:41] op_sel_hi:[1,0,1]
	v_pk_fma_f32 v[20:21], v[56:57], v[4:5], v[24:25] op_sel_hi:[1,0,1]
	v_pk_fma_f32 v[22:23], v[74:75], v[4:5], v[42:43] op_sel_hi:[1,0,1]
	v_pk_fma_f32 v[24:25], v[58:59], v[4:5], v[26:27] op_sel_hi:[1,0,1]
	v_pk_fma_f32 v[26:27], v[76:77], v[4:5], v[44:45] op_sel_hi:[1,0,1]
	v_pk_fma_f32 v[28:29], v[60:61], v[4:5], v[28:29] op_sel_hi:[1,0,1]
	v_pk_fma_f32 v[34:35], v[78:79], v[4:5], v[46:47] op_sel_hi:[1,0,1]
	v_pk_fma_f32 v[30:31], v[62:63], v[4:5], v[30:31] op_sel_hi:[1,0,1]
	v_pk_fma_f32 v[36:37], v[80:81], v[4:5], v[48:49] op_sel_hi:[1,0,1]
	v_pk_fma_f32 v[4:5], v[64:65], v[4:5], v[32:33] op_sel_hi:[1,0,1]
	s_setprio 0
	v_mul_u32_u24_e32 v3, 0x88, v198
	v_and_b32_e32 v32, -8, v199
	v_cvt_pk_bf16_f32 v6, v6, v7
	v_cvt_pk_bf16_f32 v7, v10, v11
	v_add3_u32 v3, s37, v3, v32
	v_cvt_pk_bf16_f32 v10, v14, v15
	v_cvt_pk_bf16_f32 v11, v18, v19
	v_cvt_pk_bf16_f32 v8, v8, v9
	v_cvt_pk_bf16_f32 v9, v12, v13
	ds_write2_b64 v3, v[6:7], v[10:11] offset1:2
	v_cvt_pk_bf16_f32 v6, v16, v17
	v_cvt_pk_bf16_f32 v7, v20, v21
	ds_write2_b64 v3, v[8:9], v[6:7] offset0:8 offset1:10
	v_cvt_pk_bf16_f32 v6, v22, v23
	v_cvt_pk_bf16_f32 v7, v26, v27
	v_cvt_pk_bf16_f32 v10, v34, v35
	v_cvt_pk_bf16_f32 v11, v36, v37
	v_cvt_pk_bf16_f32 v8, v24, v25
	v_cvt_pk_bf16_f32 v9, v28, v29
	ds_write2_b64 v3, v[6:7], v[10:11] offset0:4 offset1:6
	v_cvt_pk_bf16_f32 v6, v30, v31
	v_cvt_pk_bf16_f32 v7, v4, v5
	v_and_b32_e32 v4, 0x70, v184
	v_mov_b32_e32 v5, v2
	ds_write2_b64 v3, v[8:9], v[6:7] offset0:12 offset1:14
	v_lshl_add_u64 v[8:9], s[0:1], 0, v[4:5]
	s_movk_i32 s0, 0x88
	v_mul_lo_u32 v3, v182, s0
	s_waitcnt lgkmcnt(0)
	v_add3_u32 v3, s37, v4, v3
	ds_read2_b64 v[4:7], v3 offset1:1
	v_ashrrev_i32_e32 v183, 31, v182
	v_lshlrev_b64 v[10:11], 11, v[182:183]
	v_lshl_add_u64 v[12:13], v[8:9], 0, v[10:11]
	ds_read2_b64 v[8:11], v3 offset0:136 offset1:137
	s_movk_i32 s0, 0x4000
	s_waitcnt lgkmcnt(1)
	global_store_dwordx4 v[12:13], v[4:7], off offset:1024
	s_nop 1
	v_add_co_u32_e32 v4, vcc, s0, v12
	s_mov_b64 s[0:1], 0
	s_nop 0
	v_addc_co_u32_e32 v5, vcc, 0, v13, vcc
	s_waitcnt lgkmcnt(0)
	global_store_dwordx4 v[4:5], v[8:11], off offset:1024
	v_add_u32_e32 v4, 0x880, v3
	ds_read2_b64 v[4:7], v4 offset1:1
	v_add_u32_e32 v3, 0xcc0, v3
	ds_read2_b64 v[8:11], v3 offset1:1
	v_add_co_u32_e32 v14, vcc, 0x8000, v12
	s_nop 1
	v_addc_co_u32_e32 v15, vcc, 0, v13, vcc
	s_waitcnt lgkmcnt(1)
	global_store_dwordx4 v[14:15], v[4:7], off offset:1024
	s_nop 1
	v_add_co_u32_e32 v4, vcc, 0xc000, v12
	s_nop 1
	v_addc_co_u32_e32 v5, vcc, 0, v13, vcc
	s_waitcnt lgkmcnt(0)
	global_store_dwordx4 v[4:5], v[8:11], off offset:1024
	s_waitcnt lgkmcnt(0)
	s_barrier

.LBB0_572:
	v_lshlrev_b32_e32 v202, 10, v3
	v_lshlrev_b32_e32 v203, 4, v198
	v_add3_u32 v69, 0, v202, v203
	ds_read_b128 v[4:7], v69
	ds_read_b128 v[8:11], v69 offset:512
	s_mov_b32 s0, 0xf149f2ca
	v_ashrrev_i32_e32 v182, 3, v68
	s_waitcnt lgkmcnt(1)
	v_mfma_f32_32x32x16_bf16 v[52:67], v[4:7], v[158:161], 0
	s_cmp_lt_i32 s82, 0
	s_waitcnt lgkmcnt(0)
	v_mfma_f32_32x32x16_bf16 v[36:51], v[8:11], v[158:161], 0
	ds_read_b128 v[4:7], v69 offset:2048
	ds_read_b128 v[8:11], v69 offset:2560
	s_waitcnt lgkmcnt(1)
	v_mfma_f32_32x32x16_bf16 v[52:67], v[4:7], v[154:157], v[52:67]
	s_waitcnt lgkmcnt(0)
	v_mfma_f32_32x32x16_bf16 v[36:51], v[8:11], v[154:157], v[36:51]
	ds_read_b128 v[4:7], v69 offset:4096
	ds_read_b128 v[8:11], v69 offset:4608
	s_waitcnt lgkmcnt(1)
	v_mfma_f32_32x32x16_bf16 v[52:67], v[4:7], v[150:153], v[52:67]
	s_waitcnt lgkmcnt(0)
	v_mfma_f32_32x32x16_bf16 v[36:51], v[8:11], v[150:153], v[36:51]
	ds_read_b128 v[4:7], v69 offset:6144
	ds_read_b128 v[8:11], v69 offset:6656
	s_waitcnt lgkmcnt(1)
	v_mfma_f32_32x32x16_bf16 v[52:67], v[4:7], v[146:149], v[52:67]
	s_waitcnt lgkmcnt(0)
	v_mfma_f32_32x32x16_bf16 v[36:51], v[8:11], v[146:149], v[36:51]
	ds_read_b128 v[4:7], v69 offset:16384
	ds_read_b128 v[8:11], v69 offset:16896
	ds_read_b128 v[74:77], v69 offset:18432
	ds_read_b128 v[78:81], v69 offset:18944
	s_waitcnt lgkmcnt(3)
	v_mfma_f32_32x32x16_bf16 v[20:35], v[4:7], v[158:161], 0
	s_waitcnt lgkmcnt(2)
	v_mfma_f32_32x32x16_bf16 v[4:19], v[8:11], v[158:161], 0
	s_waitcnt lgkmcnt(1)
	v_mfma_f32_32x32x16_bf16 v[20:35], v[74:77], v[154:157], v[20:35]
	s_waitcnt lgkmcnt(0)
	v_mfma_f32_32x32x16_bf16 v[4:19], v[78:81], v[154:157], v[4:19]
	ds_read_b128 v[74:77], v69 offset:20480
	ds_read_b128 v[78:81], v69 offset:20992
	s_waitcnt lgkmcnt(1)
	v_mfma_f32_32x32x16_bf16 v[20:35], v[74:77], v[150:153], v[20:35]
	s_waitcnt lgkmcnt(0)
	v_mfma_f32_32x32x16_bf16 v[4:19], v[78:81], v[150:153], v[4:19]
	ds_read_b128 v[74:77], v69 offset:22528
	ds_read_b128 v[78:81], v69 offset:23040
	v_lshlrev_b32_e32 v69, 6, v3
	v_sub_u32_e32 v69, v72, v69
	v_subrev_u32_e32 v72, 31, v69
	v_cmp_lt_i32_e32 vcc, -1, v72
	s_nop 1
	v_cndmask_b32_e32 v52, v195, v52, vcc
	v_cmp_lt_i32_e32 vcc, 15, v72
	s_waitcnt lgkmcnt(1)
	v_mfma_f32_32x32x16_bf16 v[20:35], v[74:77], v[146:149], v[20:35]
	v_cndmask_b32_e32 v53, v195, v53, vcc
	v_cmp_lt_i32_e32 vcc, 31, v72
	v_max3_f32 v69, v52, s0, v53
	s_movk_i32 s0, 0x7f
	v_cndmask_b32_e32 v54, v195, v54, vcc
	v_cmp_lt_i32_e32 vcc, 47, v72
	s_waitcnt lgkmcnt(0)
	v_mfma_f32_32x32x16_bf16 v[4:19], v[78:81], v[146:149], v[4:19]
	v_cndmask_b32_e32 v55, v195, v55, vcc
	v_cmp_lt_i32_e32 vcc, s0, v72
	s_movk_i32 s0, 0x8f
	v_max3_f32 v69, v69, v54, v55
	v_cndmask_b32_e32 v73, v195, v56, vcc
	v_cmp_lt_i32_e32 vcc, s0, v72
	s_movk_i32 s0, 0x9f
	s_nop 0
	v_cndmask_b32_e32 v74, v195, v57, vcc
	v_cmp_lt_i32_e32 vcc, s0, v72
	s_movk_i32 s0, 0xaf
	v_max3_f32 v56, v69, v73, v74
	v_cndmask_b32_e32 v75, v195, v58, vcc
	v_cmp_lt_i32_e32 vcc, s0, v72
	s_movk_i32 s0, 0xff
	s_nop 0
	v_cndmask_b32_e32 v76, v195, v59, vcc
	v_cmp_lt_i32_e32 vcc, s0, v72
	s_movk_i32 s0, 0x10f
	v_max3_f32 v56, v56, v75, v76
	v_cndmask_b32_e32 v77, v195, v60, vcc
	v_cmp_lt_i32_e32 vcc, s0, v72
	s_movk_i32 s0, 0x11f
	s_nop 0
	v_cndmask_b32_e32 v78, v195, v61, vcc
	v_cmp_lt_i32_e32 vcc, s0, v72
	s_movk_i32 s0, 0x12f
	v_max3_f32 v56, v56, v77, v78
	v_cndmask_b32_e32 v79, v195, v62, vcc
	v_cmp_lt_i32_e32 vcc, s0, v72
	s_movk_i32 s0, 0x17f
	s_nop 0
	v_cndmask_b32_e32 v80, v195, v63, vcc
	v_cmp_lt_i32_e32 vcc, s0, v72
	s_movk_i32 s0, 0x18f
	v_max3_f32 v56, v56, v79, v80
	v_cndmask_b32_e32 v81, v195, v64, vcc
	v_cmp_lt_i32_e32 vcc, s0, v72
	s_movk_i32 s0, 0x19f
	s_nop 0
	v_cndmask_b32_e32 v82, v195, v65, vcc
	v_cmp_lt_i32_e32 vcc, s0, v72
	s_movk_i32 s0, 0x1af
	v_max3_f32 v56, v56, v81, v82
	v_cndmask_b32_e32 v83, v195, v66, vcc
	v_cmp_lt_i32_e32 vcc, s0, v72
	s_movk_i32 s0, 0x1ff
	s_nop 0
	v_cndmask_b32_e32 v84, v195, v67, vcc
	v_cmp_lt_i32_e32 vcc, s0, v72
	s_movk_i32 s0, 0x20f
	v_max3_f32 v56, v56, v83, v84
	v_cndmask_b32_e32 v36, v195, v36, vcc
	v_cmp_lt_i32_e32 vcc, s0, v72
	s_movk_i32 s0, 0x21f
	s_nop 0
	v_cndmask_b32_e32 v37, v195, v37, vcc
	v_cmp_lt_i32_e32 vcc, s0, v72
	s_movk_i32 s0, 0x22f
	v_max3_f32 v56, v56, v36, v37
	v_cndmask_b32_e32 v38, v195, v38, vcc
	v_cmp_lt_i32_e32 vcc, s0, v72
	s_movk_i32 s0, 0x27f
	s_nop 0
	v_cndmask_b32_e32 v39, v195, v39, vcc
	v_cmp_lt_i32_e32 vcc, s0, v72
	s_movk_i32 s0, 0x28f
	v_max3_f32 v56, v56, v38, v39
	v_cndmask_b32_e32 v40, v195, v40, vcc
	v_cmp_lt_i32_e32 vcc, s0, v72
	s_movk_i32 s0, 0x29f
	s_nop 0
	v_cndmask_b32_e32 v41, v195, v41, vcc
	v_cmp_lt_i32_e32 vcc, s0, v72
	s_movk_i32 s0, 0x2af
	v_max3_f32 v56, v56, v40, v41
	v_cndmask_b32_e32 v42, v195, v42, vcc
	v_cmp_lt_i32_e32 vcc, s0, v72
	s_movk_i32 s0, 0x2ff
	s_nop 0
	v_cndmask_b32_e32 v43, v195, v43, vcc
	v_cmp_lt_i32_e32 vcc, s0, v72
	s_movk_i32 s0, 0x30f
	v_max3_f32 v56, v56, v42, v43
	v_cndmask_b32_e32 v44, v195, v44, vcc
	v_cmp_lt_i32_e32 vcc, s0, v72
	s_movk_i32 s0, 0x31f
	s_nop 0
	v_cndmask_b32_e32 v45, v195, v45, vcc
	v_cmp_lt_i32_e32 vcc, s0, v72
	s_movk_i32 s0, 0x32f
	v_max3_f32 v56, v56, v44, v45
	v_cndmask_b32_e32 v46, v195, v46, vcc
	v_cmp_lt_i32_e32 vcc, s0, v72
	s_movk_i32 s0, 0x37f
	s_nop 0
	v_cndmask_b32_e32 v47, v195, v47, vcc
	v_cmp_lt_i32_e32 vcc, s0, v72
	s_movk_i32 s0, 0x38f
	v_max3_f32 v56, v56, v46, v47
	v_cndmask_b32_e32 v48, v195, v48, vcc
	v_cmp_lt_i32_e32 vcc, s0, v72
	s_movk_i32 s0, 0x39f
	s_nop 0
	v_cndmask_b32_e32 v49, v195, v49, vcc
	v_cmp_lt_i32_e32 vcc, s0, v72
	s_movk_i32 s0, 0x3af
	v_max3_f32 v56, v56, v48, v49
	v_cndmask_b32_e32 v50, v195, v50, vcc
	v_cmp_lt_i32_e32 vcc, s0, v72
	s_movk_i32 s0, 0x40f
	s_nop 0
	v_cndmask_b32_e32 v51, v195, v51, vcc
	v_cmp_lt_i32_e32 vcc, s39, v72
	v_max3_f32 v56, v56, v50, v51
	s_nop 0
	v_cndmask_b32_e32 v85, v195, v20, vcc
	v_cmp_lt_i32_e32 vcc, s0, v72
	s_movk_i32 s0, 0x41f
	s_nop 0
	v_cndmask_b32_e32 v86, v195, v21, vcc
	v_cmp_lt_i32_e32 vcc, s0, v72
	s_movk_i32 s0, 0x42f
	v_max3_f32 v20, v56, v85, v86
	v_cndmask_b32_e32 v87, v195, v22, vcc
	v_cmp_lt_i32_e32 vcc, s0, v72
	s_movk_i32 s0, 0x47f
	s_nop 0
	v_cndmask_b32_e32 v88, v195, v23, vcc
	v_cmp_lt_i32_e32 vcc, s0, v72
	s_movk_i32 s0, 0x48f
	v_max3_f32 v20, v20, v87, v88
	v_cndmask_b32_e32 v89, v195, v24, vcc
	v_cmp_lt_i32_e32 vcc, s0, v72
	s_movk_i32 s0, 0x49f
	s_nop 0
	v_cndmask_b32_e32 v90, v195, v25, vcc
	v_cmp_lt_i32_e32 vcc, s0, v72
	s_movk_i32 s0, 0x4af
	v_max3_f32 v20, v20, v89, v90
	v_cndmask_b32_e32 v91, v195, v26, vcc
	v_cmp_lt_i32_e32 vcc, s0, v72
	s_movk_i32 s0, 0x4ff
	s_nop 0
	v_cndmask_b32_e32 v92, v195, v27, vcc
	v_cmp_lt_i32_e32 vcc, s0, v72
	s_movk_i32 s0, 0x50f
	v_max3_f32 v20, v20, v91, v92
	v_cndmask_b32_e32 v93, v195, v28, vcc
	v_cmp_lt_i32_e32 vcc, s0, v72
	s_movk_i32 s0, 0x51f
	s_nop 0
	v_cndmask_b32_e32 v94, v195, v29, vcc
	v_cmp_lt_i32_e32 vcc, s0, v72
	s_movk_i32 s0, 0x52f
	v_max3_f32 v20, v20, v93, v94
	v_cndmask_b32_e32 v95, v195, v30, vcc
	v_cmp_lt_i32_e32 vcc, s0, v72
	s_movk_i32 s0, 0x57f
	s_nop 0
	v_cndmask_b32_e32 v96, v195, v31, vcc
	v_cmp_lt_i32_e32 vcc, s0, v72
	s_movk_i32 s0, 0x58f
	v_max3_f32 v20, v20, v95, v96
	v_cndmask_b32_e32 v97, v195, v32, vcc
	v_cmp_lt_i32_e32 vcc, s0, v72
	s_movk_i32 s0, 0x59f
	s_nop 0
	v_cndmask_b32_e32 v98, v195, v33, vcc
	v_cmp_lt_i32_e32 vcc, s0, v72
	s_movk_i32 s0, 0x5af
	v_max3_f32 v20, v20, v97, v98
	v_cndmask_b32_e32 v99, v195, v34, vcc
	v_cmp_lt_i32_e32 vcc, s0, v72
	s_movk_i32 s0, 0x5ff
	s_nop 0
	v_cndmask_b32_e32 v100, v195, v35, vcc
	v_cmp_lt_i32_e32 vcc, s0, v72
	s_movk_i32 s0, 0x60f
	v_max3_f32 v20, v20, v99, v100
	v_cndmask_b32_e32 v101, v195, v4, vcc
	v_cmp_lt_i32_e32 vcc, s0, v72
	s_movk_i32 s0, 0x61f
	s_nop 0
	v_cndmask_b32_e32 v102, v195, v5, vcc
	v_cmp_lt_i32_e32 vcc, s0, v72
	s_movk_i32 s0, 0x62f
	v_max3_f32 v4, v20, v101, v102
	v_cndmask_b32_e32 v103, v195, v6, vcc
	v_cmp_lt_i32_e32 vcc, s0, v72
	s_movk_i32 s0, 0x67f
	s_nop 0
	v_cndmask_b32_e32 v104, v195, v7, vcc
	v_cmp_lt_i32_e32 vcc, s0, v72
	s_movk_i32 s0, 0x68f
	v_max3_f32 v4, v4, v103, v104
	v_cndmask_b32_e32 v58, v195, v8, vcc
	v_cmp_lt_i32_e32 vcc, s0, v72
	s_movk_i32 s0, 0x69f
	s_nop 0
	v_cndmask_b32_e32 v59, v195, v9, vcc
	v_cmp_lt_i32_e32 vcc, s0, v72
	s_movk_i32 s0, 0x6af
	v_max3_f32 v4, v4, v58, v59
	v_cndmask_b32_e32 v56, v195, v10, vcc
	v_cmp_lt_i32_e32 vcc, s0, v72
	s_movk_i32 s0, 0x6ff
	s_nop 0
	v_cndmask_b32_e32 v57, v195, v11, vcc
	v_cmp_lt_i32_e32 vcc, s0, v72
	s_movk_i32 s0, 0x70f
	v_max3_f32 v4, v4, v56, v57
	v_cndmask_b32_e32 v62, v195, v12, vcc
	v_cmp_lt_i32_e32 vcc, s0, v72
	s_movk_i32 s0, 0x71f
	s_nop 0
	v_cndmask_b32_e32 v63, v195, v13, vcc
	v_cmp_lt_i32_e32 vcc, s0, v72
	s_movk_i32 s0, 0x72f
	v_max3_f32 v4, v4, v62, v63
	v_cndmask_b32_e32 v60, v195, v14, vcc
	v_cmp_lt_i32_e32 vcc, s0, v72
	s_movk_i32 s0, 0x77f
	s_nop 0
	v_cndmask_b32_e32 v61, v195, v15, vcc
	v_cmp_lt_i32_e32 vcc, s0, v72
	s_movk_i32 s0, 0x78f
	v_max3_f32 v4, v4, v60, v61
	v_cndmask_b32_e32 v69, v195, v16, vcc
	v_cmp_lt_i32_e32 vcc, s0, v72
	s_movk_i32 s0, 0x79f
	s_nop 0
	v_cndmask_b32_e32 v66, v195, v17, vcc
	v_cmp_lt_i32_e32 vcc, s0, v72
	s_movk_i32 s0, 0x7af
	v_max3_f32 v4, v4, v69, v66
	v_cndmask_b32_e32 v65, v195, v18, vcc
	v_cmp_lt_i32_e32 vcc, s0, v72
	s_mov_b32 s0, 0xefa18f08
	s_nop 0
	v_cndmask_b32_e32 v64, v195, v19, vcc
	v_max3_f32 v4, v4, v65, v64
	v_mov_b32_e32 v5, v4
	s_nop 1
	v_permlane32_swap_b32_e32 v4, v5
	v_max3_f32 v67, v4, v5, s0
	v_sub_f32_e32 v4, v52, v67
	v_exp_f32_e32 v4, v4
	v_sub_f32_e32 v5, v53, v67
	v_exp_f32_e32 v5, v5
	v_sub_f32_e32 v9, v73, v67
	v_add_f32_e32 v6, 0, v4
	v_exp_f32_e32 v10, v9
	v_add_f32_e32 v7, v5, v6
	v_sub_f32_e32 v6, v54, v67
	v_exp_f32_e32 v6, v6
	v_sub_f32_e32 v9, v74, v67
	v_exp_f32_e32 v11, v9
	v_sub_f32_e32 v13, v77, v67
	v_add_f32_e32 v8, v6, v7
	v_sub_f32_e32 v7, v55, v67
	v_exp_f32_e32 v7, v7
	v_exp_f32_e32 v14, v13
	v_sub_f32_e32 v13, v78, v67
	v_exp_f32_e32 v15, v13
	v_add_f32_e32 v8, v7, v8
	v_add_f32_e32 v8, v10, v8
	v_add_f32_e32 v9, v11, v8
	v_sub_f32_e32 v8, v75, v67
	v_exp_f32_e32 v8, v8
	v_sub_f32_e32 v17, v81, v67
	v_exp_f32_e32 v18, v17
	v_sub_f32_e32 v17, v82, v67
	v_add_f32_e32 v12, v8, v9
	v_sub_f32_e32 v9, v76, v67
	v_exp_f32_e32 v9, v9
	v_exp_f32_e32 v19, v17
	v_sub_f32_e32 v21, v36, v67
	v_exp_f32_e32 v22, v21
	v_add_f32_e32 v12, v9, v12
	v_add_f32_e32 v12, v14, v12
	v_add_f32_e32 v13, v15, v12
	v_sub_f32_e32 v12, v79, v67
	v_exp_f32_e32 v12, v12
	v_sub_f32_e32 v21, v37, v67
	v_exp_f32_e32 v23, v21
	v_sub_f32_e32 v25, v40, v67
	v_add_f32_e32 v16, v12, v13
	v_sub_f32_e32 v13, v80, v67
	v_exp_f32_e32 v13, v13
	v_exp_f32_e32 v26, v25
	v_sub_f32_e32 v25, v41, v67
	v_exp_f32_e32 v27, v25
	v_add_f32_e32 v16, v13, v16
	v_add_f32_e32 v16, v18, v16
	v_add_f32_e32 v17, v19, v16
	v_sub_f32_e32 v16, v83, v67
	v_exp_f32_e32 v16, v16
	v_sub_f32_e32 v29, v44, v67
	v_exp_f32_e32 v30, v29
	v_sub_f32_e32 v29, v45, v67
	v_add_f32_e32 v20, v16, v17
	v_sub_f32_e32 v17, v84, v67
	v_exp_f32_e32 v17, v17
	v_exp_f32_e32 v31, v29
	v_sub_f32_e32 v33, v48, v67
	v_exp_f32_e32 v34, v33
	v_add_f32_e32 v20, v17, v20
	v_add_f32_e32 v20, v22, v20
	v_add_f32_e32 v21, v23, v20
	v_sub_f32_e32 v20, v38, v67
	v_exp_f32_e32 v20, v20
	v_sub_f32_e32 v33, v49, v67
	v_exp_f32_e32 v35, v33
	v_sub_f32_e32 v37, v85, v67
	v_add_f32_e32 v24, v20, v21
	v_sub_f32_e32 v21, v39, v67
	v_exp_f32_e32 v21, v21
	v_exp_f32_e32 v38, v37
	v_sub_f32_e32 v37, v86, v67
	v_exp_f32_e32 v39, v37
	v_add_f32_e32 v24, v21, v24
	v_add_f32_e32 v24, v26, v24
	v_add_f32_e32 v25, v27, v24
	v_sub_f32_e32 v24, v42, v67
	v_exp_f32_e32 v24, v24
	v_sub_f32_e32 v41, v89, v67
	v_exp_f32_e32 v42, v41
	v_sub_f32_e32 v41, v90, v67
	v_add_f32_e32 v28, v24, v25
	v_sub_f32_e32 v25, v43, v67
	v_exp_f32_e32 v25, v25
	v_exp_f32_e32 v43, v41
	v_sub_f32_e32 v45, v93, v67
	v_sub_f32_e32 v49, v97, v67
	v_add_f32_e32 v28, v25, v28
	v_add_f32_e32 v28, v30, v28
	v_add_f32_e32 v29, v31, v28
	v_sub_f32_e32 v28, v46, v67
	v_exp_f32_e32 v28, v28
	v_exp_f32_e32 v46, v45
	v_sub_f32_e32 v45, v94, v67
	v_sub_f32_e32 v53, v101, v67
	v_add_f32_e32 v32, v28, v29
	v_sub_f32_e32 v29, v47, v67
	v_exp_f32_e32 v29, v29
	v_exp_f32_e32 v47, v45
	v_exp_f32_e32 v54, v53
	v_sub_f32_e32 v53, v102, v67
	v_add_f32_e32 v32, v29, v32
	v_add_f32_e32 v32, v34, v32
	v_add_f32_e32 v33, v35, v32
	v_sub_f32_e32 v32, v50, v67
	v_exp_f32_e32 v32, v32
	v_exp_f32_e32 v50, v49
	v_sub_f32_e32 v49, v98, v67
	v_exp_f32_e32 v55, v53
	v_add_f32_e32 v36, v32, v33
	v_sub_f32_e32 v33, v51, v67
	v_exp_f32_e32 v33, v33
	v_exp_f32_e32 v51, v49
	v_sub_f32_e32 v58, v58, v67
	v_exp_f32_e32 v58, v58
	v_add_f32_e32 v36, v33, v36
	v_add_f32_e32 v36, v38, v36
	v_add_f32_e32 v37, v39, v36
	v_sub_f32_e32 v36, v87, v67
	v_exp_f32_e32 v36, v36
	v_sub_f32_e32 v59, v59, v67
	v_exp_f32_e32 v59, v59
	v_sub_f32_e32 v56, v56, v67
	v_add_f32_e32 v40, v36, v37
	v_sub_f32_e32 v37, v88, v67
	v_exp_f32_e32 v37, v37
	v_exp_f32_e32 v56, v56
	v_sub_f32_e32 v57, v57, v67
	v_exp_f32_e32 v57, v57
	v_add_f32_e32 v40, v37, v40
	v_add_f32_e32 v40, v42, v40
	v_add_f32_e32 v41, v43, v40
	v_sub_f32_e32 v40, v91, v67
	v_exp_f32_e32 v40, v40
	v_sub_f32_e32 v62, v62, v67
	v_exp_f32_e32 v62, v62
	v_sub_f32_e32 v63, v63, v67
	v_add_f32_e32 v44, v40, v41
	v_sub_f32_e32 v41, v92, v67
	v_exp_f32_e32 v41, v41
	v_exp_f32_e32 v63, v63
	v_sub_f32_e32 v60, v60, v67
	v_exp_f32_e32 v60, v60
	v_add_f32_e32 v44, v41, v44
	v_add_f32_e32 v44, v46, v44
	v_add_f32_e32 v45, v47, v44
	v_sub_f32_e32 v44, v95, v67
	v_exp_f32_e32 v44, v44
	v_sub_f32_e32 v61, v61, v67
	v_exp_f32_e32 v61, v61
	v_sub_f32_e32 v69, v69, v67
	v_add_f32_e32 v48, v44, v45
	v_sub_f32_e32 v45, v96, v67
	v_exp_f32_e32 v45, v45
	v_sub_f32_e32 v66, v66, v67
	v_sub_f32_e32 v65, v65, v67
	v_sub_f32_e32 v64, v64, v67
	v_add_f32_e32 v48, v45, v48
	v_add_f32_e32 v48, v50, v48
	v_add_f32_e32 v49, v51, v48
	v_sub_f32_e32 v48, v99, v67
	v_exp_f32_e32 v48, v48
	s_nop 0
	v_add_f32_e32 v52, v48, v49
	v_sub_f32_e32 v49, v100, v67
	v_exp_f32_e32 v49, v49
	s_nop 0
	v_add_f32_e32 v52, v49, v52
	v_add_f32_e32 v52, v54, v52
	v_add_f32_e32 v53, v55, v52
	v_sub_f32_e32 v52, v103, v67
	v_exp_f32_e32 v52, v52
	s_nop 0
	v_add_f32_e32 v72, v52, v53
	v_sub_f32_e32 v53, v104, v67
	v_exp_f32_e32 v53, v53
	v_exp_f32_e32 v67, v64
	v_add_f32_e32 v72, v53, v72
	v_add_f32_e32 v72, v58, v72
	v_add_f32_e32 v72, v59, v72
	v_add_f32_e32 v72, v56, v72
	v_add_f32_e32 v72, v57, v72
	v_add_f32_e32 v72, v62, v72
	v_add_f32_e32 v72, v63, v72
	v_add_f32_e32 v72, v60, v72
	v_add_f32_e32 v73, v61, v72
	v_exp_f32_e32 v72, v69
	s_nop 0
	v_add_f32_e32 v69, v72, v73
	v_exp_f32_e32 v73, v66
	v_exp_f32_e32 v66, v65
	v_add_f32_e32 v69, v73, v69
	v_add_f32_e32 v65, v66, v69
	v_add_f32_e32 v64, v67, v65
	v_mov_b32_e32 v65, v64
	s_nop 1
	v_permlane32_swap_b32_e32 v64, v65
	v_add_f32_e32 v64, v64, v65
	v_div_scale_f32 v65, s[2:3], v64, v64, 1.0
	v_rcp_f32_e32 v69, v65
	v_cmp_lt_f32_e64 s[0:1], 0, v64
	v_fma_f32 v74, -v65, v69, 1.0
	v_fmac_f32_e32 v69, v74, v69
	v_div_scale_f32 v74, vcc, 1.0, v64, 1.0
	v_mul_f32_e32 v75, v74, v69
	v_fma_f32 v76, -v65, v75, v74
	v_fmac_f32_e32 v75, v76, v69
	v_fma_f32 v65, -v65, v75, v74
	v_div_fmas_f32 v65, v65, v69, v75
	v_and_b32_e32 v69, 64, v212
	v_div_fixup_f32 v64, v65, v64, 1.0
	v_xor_b32_e32 v65, 32, v212
	v_add_u32_e32 v69, 64, v69
	v_cmp_lt_i32_e32 vcc, v65, v69
	v_cndmask_b32_e64 v76, 0, v64, s[0:1]
	v_add_u32_e32 v64, s12, v71
	v_cndmask_b32_e32 v65, v212, v65, vcc
	v_lshlrev_b32_e32 v77, 2, v65
	v_pk_mul_f32 v[6:7], v[6:7], v[76:77] op_sel_hi:[1,0]
	ds_bpermute_b32 v74, v77, v7
	v_mul_lo_u32 v64, v64, s64
	v_lshlrev_b32_e32 v69, 2, v3
	v_add3_u32 v88, s33, v64, v69
	v_pk_mul_f32 v[64:65], v[4:5], v[76:77] op_sel_hi:[1,0]
	v_cmp_gt_u32_e32 vcc, 32, v68
	v_pk_mul_f32 v[4:5], v[70:71], v[64:65] op_sel_hi:[0,1]
	v_add_f32_e32 v75, v6, v7
	v_add_f32_e32 v64, v64, v65
	v_add_f32_e32 v64, v64, v75
	s_waitcnt lgkmcnt(0)
	v_cndmask_b32_e64 v65, v74, 0, vcc
	v_pk_mul_f32 v[8:9], v[8:9], v[76:77] op_sel_hi:[1,0]
	v_add_f32_e32 v64, v65, v64
	ds_bpermute_b32 v65, v77, v9
	v_pk_mul_f32 v[10:11], v[10:11], v[76:77] op_sel_hi:[1,0]
	v_add_f32_e32 v75, v8, v9
	v_pk_mul_f32 v[78:79], v[70:71], v[10:11] op_sel_hi:[0,1]
	v_add_f32_e32 v10, v10, v11
	v_add_f32_e32 v10, v10, v75
	s_waitcnt lgkmcnt(0)
	v_cndmask_b32_e32 v11, v65, v74, vcc
	v_add_f32_e32 v10, v11, v10
	ds_write2_b32 v88, v64, v10 offset1:2
	v_pk_mul_f32 v[10:11], v[12:13], v[76:77] op_sel_hi:[1,0]
	ds_bpermute_b32 v12, v77, v11
	v_add_f32_e32 v13, v10, v11
	v_pk_mul_f32 v[84:85], v[70:71], v[10:11] op_sel_hi:[0,1]
	v_pk_mul_f32 v[10:11], v[16:17], v[76:77] op_sel_hi:[1,0]
	v_pk_mul_f32 v[80:81], v[70:71], v[8:9] op_sel_hi:[0,1]
	v_pk_mul_f32 v[8:9], v[14:15], v[76:77] op_sel_hi:[1,0]
	ds_bpermute_b32 v14, v77, v11
	v_pk_mul_f32 v[82:83], v[70:71], v[8:9] op_sel_hi:[0,1]
	v_add_f32_e32 v8, v8, v9
	v_add_f32_e32 v8, v8, v13
	s_waitcnt lgkmcnt(1)
	v_cndmask_b32_e32 v9, v12, v65, vcc
	v_add_f32_e32 v13, v9, v8
	v_pk_mul_f32 v[8:9], v[18:19], v[76:77] op_sel_hi:[1,0]
	v_add_f32_e32 v15, v10, v11
	v_pk_mul_f32 v[86:87], v[70:71], v[10:11] op_sel_hi:[0,1]
	v_pk_mul_f32 v[10:11], v[20:21], v[76:77] op_sel_hi:[1,0]
	v_pk_mul_f32 v[18:19], v[70:71], v[8:9] op_sel_hi:[0,1]
	v_add_f32_e32 v8, v8, v9
	s_waitcnt lgkmcnt(0)
	v_cndmask_b32_e32 v9, v14, v12, vcc
	ds_bpermute_b32 v12, v77, v11
	v_add_f32_e32 v8, v8, v15
	v_add_f32_e32 v8, v9, v8
	ds_write2_b32 v88, v13, v8 offset0:4 offset1:6
	v_pk_mul_f32 v[8:9], v[22:23], v[76:77] op_sel_hi:[1,0]
	v_add_f32_e32 v13, v10, v11
	v_pk_mul_f32 v[20:21], v[70:71], v[10:11] op_sel_hi:[0,1]
	v_pk_mul_f32 v[10:11], v[24:25], v[76:77] op_sel_hi:[1,0]
	v_pk_mul_f32 v[22:23], v[70:71], v[8:9] op_sel_hi:[0,1]
	v_add_f32_e32 v8, v8, v9
	s_waitcnt lgkmcnt(1)
	v_cndmask_b32_e32 v9, v12, v14, vcc
	ds_bpermute_b32 v14, v77, v11
	v_add_f32_e32 v8, v8, v13
	v_add_f32_e32 v13, v8, v9
	v_pk_mul_f32 v[8:9], v[26:27], v[76:77] op_sel_hi:[1,0]
	v_add_f32_e32 v15, v10, v11
	v_pk_mul_f32 v[24:25], v[70:71], v[10:11] op_sel_hi:[0,1]
	v_pk_mul_f32 v[10:11], v[28:29], v[76:77] op_sel_hi:[1,0]
	v_pk_mul_f32 v[26:27], v[70:71], v[8:9] op_sel_hi:[0,1]
	v_add_f32_e32 v8, v8, v9
	s_waitcnt lgkmcnt(0)
	v_cndmask_b32_e32 v9, v14, v12, vcc
	ds_bpermute_b32 v12, v77, v11
	v_add_f32_e32 v8, v8, v15
	v_add_f32_e32 v8, v8, v9
	ds_write2_b32 v88, v13, v8 offset0:8 offset1:10
	v_pk_mul_f32 v[8:9], v[30:31], v[76:77] op_sel_hi:[1,0]
	v_add_f32_e32 v13, v10, v11
	v_pk_mul_f32 v[28:29], v[70:71], v[10:11] op_sel_hi:[0,1]
	v_pk_mul_f32 v[10:11], v[32:33], v[76:77] op_sel_hi:[1,0]
	v_pk_mul_f32 v[30:31], v[70:71], v[8:9] op_sel_hi:[0,1]
	v_add_f32_e32 v8, v8, v9
	s_waitcnt lgkmcnt(1)
	v_cndmask_b32_e32 v9, v12, v14, vcc
	ds_bpermute_b32 v14, v77, v11
	v_add_f32_e32 v8, v8, v13
	v_add_f32_e32 v13, v8, v9
	v_pk_mul_f32 v[8:9], v[34:35], v[76:77] op_sel_hi:[1,0]
	v_add_f32_e32 v15, v10, v11
	v_pk_mul_f32 v[34:35], v[70:71], v[8:9] op_sel_hi:[0,1]
	v_add_f32_e32 v8, v8, v9
	v_add_f32_e32 v8, v8, v15
	s_waitcnt lgkmcnt(0)
	v_cndmask_b32_e32 v9, v14, v12, vcc
	v_add_f32_e32 v8, v8, v9
	ds_write2_b32 v88, v13, v8 offset0:12 offset1:14
	v_pk_mul_f32 v[12:13], v[36:37], v[76:77] op_sel_hi:[1,0]
	ds_bpermute_b32 v36, v77, v13
	v_pk_mul_f32 v[16:17], v[40:41], v[76:77] op_sel_hi:[1,0]
	ds_bpermute_b32 v40, v77, v17
	v_pk_mul_f32 v[32:33], v[70:71], v[10:11] op_sel_hi:[0,1]
	v_pk_mul_f32 v[10:11], v[38:39], v[76:77] op_sel_hi:[1,0]
	v_add_f32_e32 v15, v12, v13
	v_pk_mul_f32 v[8:9], v[70:71], v[10:11] op_sel_hi:[0,1]
	v_add_f32_e32 v10, v10, v11
	v_add_f32_e32 v10, v10, v15
	s_waitcnt lgkmcnt(1)
	v_cndmask_b32_e32 v11, v36, v14, vcc
	v_pk_mul_f32 v[14:15], v[42:43], v[76:77] op_sel_hi:[1,0]
	v_add_f32_e32 v37, v10, v11
	v_pk_mul_f32 v[10:11], v[70:71], v[12:13] op_sel_hi:[0,1]
	v_pk_mul_f32 v[12:13], v[70:71], v[14:15] op_sel_hi:[0,1]
	v_add_f32_e32 v38, v16, v17
	v_add_f32_e32 v14, v14, v15
	v_add_f32_e32 v14, v14, v38
	s_waitcnt lgkmcnt(0)
	v_cndmask_b32_e32 v15, v40, v36, vcc
	v_pk_mul_f32 v[38:39], v[44:45], v[76:77] op_sel_hi:[1,0]
	v_add_f32_e32 v14, v14, v15
	ds_bpermute_b32 v41, v77, v39
	ds_write2_b32 v88, v37, v14 offset0:16 offset1:18
	v_pk_mul_f32 v[36:37], v[46:47], v[76:77] op_sel_hi:[1,0]
	v_pk_mul_f32 v[14:15], v[70:71], v[16:17] op_sel_hi:[0,1]
	v_pk_mul_f32 v[16:17], v[70:71], v[36:37] op_sel_hi:[0,1]
	v_add_f32_e32 v42, v38, v39
	v_add_f32_e32 v36, v36, v37
	v_pk_mul_f32 v[64:65], v[70:71], v[38:39] op_sel_hi:[0,1]
	v_pk_mul_f32 v[38:39], v[48:49], v[76:77] op_sel_hi:[1,0]
	v_add_f32_e32 v36, v36, v42
	ds_bpermute_b32 v42, v77, v39
	s_waitcnt lgkmcnt(2)
	v_cndmask_b32_e32 v37, v41, v40, vcc
	v_add_f32_e32 v40, v36, v37
	v_pk_mul_f32 v[36:37], v[50:51], v[76:77] op_sel_hi:[1,0]
	v_add_f32_e32 v43, v38, v39
	v_pk_mul_f32 v[50:51], v[70:71], v[36:37] op_sel_hi:[0,1]
	v_add_f32_e32 v36, v36, v37
	v_add_f32_e32 v36, v36, v43
	s_waitcnt lgkmcnt(0)
	v_cndmask_b32_e32 v37, v42, v41, vcc
	v_add_f32_e32 v36, v36, v37
	v_pk_mul_f32 v[74:75], v[70:71], v[38:39] op_sel_hi:[0,1]
	v_pk_mul_f32 v[38:39], v[52:53], v[76:77] op_sel_hi:[1,0]
	ds_write2_b32 v88, v40, v36 offset0:20 offset1:22
	ds_bpermute_b32 v40, v77, v39
	v_pk_mul_f32 v[36:37], v[54:55], v[76:77] op_sel_hi:[1,0]
	v_add_f32_e32 v41, v38, v39
	v_pk_mul_f32 v[52:53], v[70:71], v[38:39] op_sel_hi:[0,1]
	v_pk_mul_f32 v[38:39], v[56:57], v[76:77] op_sel_hi:[1,0]
	v_pk_mul_f32 v[54:55], v[70:71], v[36:37] op_sel_hi:[0,1]
	v_add_f32_e32 v36, v36, v37
	s_waitcnt lgkmcnt(0)
	v_cndmask_b32_e32 v37, v40, v42, vcc
	ds_bpermute_b32 v42, v77, v39
	v_add_f32_e32 v36, v36, v41
	v_add_f32_e32 v41, v36, v37
	v_pk_mul_f32 v[36:37], v[58:59], v[76:77] op_sel_hi:[1,0]
	v_add_f32_e32 v43, v38, v39
	v_pk_mul_f32 v[56:57], v[70:71], v[38:39] op_sel_hi:[0,1]
	v_pk_mul_f32 v[38:39], v[60:61], v[76:77] op_sel_hi:[1,0]
	v_pk_mul_f32 v[58:59], v[70:71], v[36:37] op_sel_hi:[0,1]
	v_add_f32_e32 v36, v36, v37
	s_waitcnt lgkmcnt(0)
	v_cndmask_b32_e32 v37, v42, v40, vcc
	ds_bpermute_b32 v40, v77, v39
	v_add_f32_e32 v36, v36, v43
	v_add_f32_e32 v36, v36, v37
	ds_write2_b32 v88, v41, v36 offset0:24 offset1:26
	v_pk_mul_f32 v[36:37], v[62:63], v[76:77] op_sel_hi:[1,0]
	v_add_f32_e32 v41, v38, v39
	v_pk_mul_f32 v[60:61], v[70:71], v[38:39] op_sel_hi:[0,1]
	v_pk_mul_f32 v[38:39], v[66:67], v[76:77] op_sel_hi:[1,0]
	v_pk_mul_f32 v[62:63], v[70:71], v[36:37] op_sel_hi:[0,1]
	v_add_f32_e32 v36, v36, v37
	s_waitcnt lgkmcnt(1)
	v_cndmask_b32_e32 v37, v40, v42, vcc
	ds_bpermute_b32 v42, v77, v39
	v_add_f32_e32 v36, v36, v41
	v_add_f32_e32 v41, v36, v37
	v_pk_mul_f32 v[36:37], v[72:73], v[76:77] op_sel_hi:[1,0]
	v_add_f32_e32 v43, v38, v39
	v_pk_mul_f32 v[72:73], v[70:71], v[36:37] op_sel_hi:[0,1]
	v_add_f32_e32 v36, v36, v37
	v_cvt_pk_bf16_f32 v78, v78, v79
	v_cvt_pk_bf16_f32 v79, v80, v81
	v_cvt_pk_bf16_f32 v80, v82, v83
	v_cvt_pk_bf16_f32 v82, v18, v19
	v_lshlrev_b32_e32 v18, 1, v68
	v_bfe_u32 v19, v68, 2, 2
	s_mov_b32 s0, 0x3fffffc
	v_add_f32_e32 v36, v36, v43
	s_waitcnt lgkmcnt(0)
	v_cndmask_b32_e32 v37, v42, v40, vcc
	v_and_b32_e32 v204, 32, v18
	v_and_or_b32 v19, v182, s0, v19
	v_add_f32_e32 v36, v36, v37
	v_add_u32_e32 v18, 0, v204
	v_lshlrev_b32_e32 v205, 6, v19
	v_pk_mul_f32 v[6:7], v[70:71], v[6:7] op_sel_hi:[0,1]
	ds_write2_b32 v88, v41, v36 offset0:28 offset1:30
	v_pk_mul_f32 v[66:67], v[70:71], v[38:39] op_sel_hi:[0,1]
	v_add3_u32 v70, v18, v201, v205
	v_cvt_pk_bf16_f32 v81, v84, v85
	v_cvt_pk_bf16_f32 v83, v86, v87
	v_cvt_pk_bf16_f32 v84, v22, v23
	v_cvt_pk_bf16_f32 v85, v20, v21
	v_cvt_pk_bf16_f32 v87, v24, v25
	ds_read_b64_tr_b16 v[18:19], v70 offset:8192
	ds_read_b64_tr_b16 v[20:21], v70 offset:8704
	ds_read_b64_tr_b16 v[22:23], v70 offset:12288
	ds_read_b64_tr_b16 v[24:25], v70 offset:12800
	v_cvt_pk_bf16_f32 v76, v4, v5
	v_cvt_pk_bf16_f32 v77, v6, v7
	v_cvt_pk_bf16_f32 v86, v26, v27
	v_cvt_pk_bf16_f32 v4, v30, v31
	v_cvt_pk_bf16_f32 v5, v28, v29
	v_cvt_pk_bf16_f32 v6, v34, v35
	v_cvt_pk_bf16_f32 v7, v32, v33
	s_waitcnt lgkmcnt(2)
	v_mfma_f32_32x32x16_bf16 v[34:49], v[18:21], v[76:79], 0
	s_waitcnt lgkmcnt(0)
	v_mfma_f32_32x32x16_bf16 v[18:33], v[22:25], v[76:79], 0
	ds_read_b64_tr_b16 v[76:77], v70 offset:9216
	ds_read_b64_tr_b16 v[78:79], v70 offset:9728
	ds_read_b64_tr_b16 v[88:89], v70 offset:13312
	ds_read_b64_tr_b16 v[90:91], v70 offset:13824
	s_waitcnt lgkmcnt(2)
	v_mfma_f32_32x32x16_bf16 v[34:49], v[76:79], v[80:83], v[34:49]
	s_waitcnt lgkmcnt(0)
	v_mfma_f32_32x32x16_bf16 v[18:33], v[88:91], v[80:83], v[18:33]
	ds_read_b64_tr_b16 v[76:77], v70 offset:10240
	ds_read_b64_tr_b16 v[78:79], v70 offset:10752
	ds_read_b64_tr_b16 v[80:81], v70 offset:14336
	ds_read_b64_tr_b16 v[82:83], v70 offset:14848
	s_waitcnt lgkmcnt(2)
	v_mfma_f32_32x32x16_bf16 v[34:49], v[76:79], v[84:87], v[34:49]
	s_waitcnt lgkmcnt(0)
	v_mfma_f32_32x32x16_bf16 v[18:33], v[80:83], v[84:87], v[18:33]
	ds_read_b64_tr_b16 v[76:77], v70 offset:11264
	ds_read_b64_tr_b16 v[78:79], v70 offset:11776
	ds_read_b64_tr_b16 v[80:81], v70 offset:15360
	ds_read_b64_tr_b16 v[82:83], v70 offset:15872
	s_waitcnt lgkmcnt(2)
	v_mfma_f32_32x32x16_bf16 v[34:49], v[76:79], v[4:7], v[34:49]
	v_cvt_pk_bf16_f32 v76, v8, v9
	v_cvt_pk_bf16_f32 v77, v10, v11
	v_cvt_pk_bf16_f32 v79, v14, v15
	v_cvt_pk_bf16_f32 v14, v50, v51
	v_cvt_pk_bf16_f32 v8, v54, v55
	v_cvt_pk_bf16_f32 v9, v52, v53
	v_cvt_pk_bf16_f32 v11, v56, v57
	s_waitcnt lgkmcnt(0)
	v_mfma_f32_32x32x16_bf16 v[18:33], v[80:83], v[4:7], v[18:33]
	ds_read_b64_tr_b16 v[50:51], v70 offset:24576
	ds_read_b64_tr_b16 v[52:53], v70 offset:25088
	ds_read_b64_tr_b16 v[54:55], v70 offset:28672
	ds_read_b64_tr_b16 v[56:57], v70 offset:29184
	v_cvt_pk_bf16_f32 v78, v12, v13
	v_cvt_pk_bf16_f32 v12, v16, v17
	v_cvt_pk_bf16_f32 v13, v64, v65
	v_cvt_pk_bf16_f32 v15, v74, v75
	v_cvt_pk_bf16_f32 v10, v58, v59
	v_cvt_pk_bf16_f32 v4, v62, v63
	s_waitcnt lgkmcnt(2)
	v_mfma_f32_32x32x16_bf16 v[34:49], v[50:53], v[76:79], v[34:49]
	v_cvt_pk_bf16_f32 v5, v60, v61
	v_cvt_pk_bf16_f32 v6, v72, v73
	v_cvt_pk_bf16_f32 v7, v66, v67
	s_waitcnt lgkmcnt(0)
	v_mfma_f32_32x32x16_bf16 v[18:33], v[54:57], v[76:79], v[18:33]
	ds_read_b64_tr_b16 v[50:51], v70 offset:25600
	ds_read_b64_tr_b16 v[52:53], v70 offset:26112
	ds_read_b64_tr_b16 v[54:55], v70 offset:29696
	ds_read_b64_tr_b16 v[56:57], v70 offset:30208
	s_waitcnt lgkmcnt(2)
	v_mfma_f32_32x32x16_bf16 v[34:49], v[50:53], v[12:15], v[34:49]
	s_waitcnt lgkmcnt(0)
	v_mfma_f32_32x32x16_bf16 v[18:33], v[54:57], v[12:15], v[18:33]
	ds_read_b64_tr_b16 v[12:13], v70 offset:26624
	ds_read_b64_tr_b16 v[14:15], v70 offset:27136
	ds_read_b64_tr_b16 v[50:51], v70 offset:30720
	ds_read_b64_tr_b16 v[52:53], v70 offset:31232
	s_waitcnt lgkmcnt(2)
	v_mfma_f32_32x32x16_bf16 v[34:49], v[12:15], v[8:11], v[34:49]
	s_waitcnt lgkmcnt(0)
	v_mfma_f32_32x32x16_bf16 v[18:33], v[50:53], v[8:11], v[18:33]
	ds_read_b64_tr_b16 v[8:9], v70 offset:27648
	ds_read_b64_tr_b16 v[10:11], v70 offset:28160
	ds_read_b64_tr_b16 v[12:13], v70 offset:31744
	ds_read_b64_tr_b16 v[14:15], v70 offset:32256
	s_waitcnt lgkmcnt(2)
	v_mfma_f32_32x32x16_bf16 v[34:49], v[8:11], v[4:7], v[34:49]
	s_waitcnt lgkmcnt(0)
	v_mfma_f32_32x32x16_bf16 v[18:33], v[12:15], v[4:7], v[18:33]
	s_cbranch_scc1 .LBB0_640
	s_cmp_gt_u32 s78, 7
	s_cselect_b64 s[94:95], -1, 0
	s_cmp_gt_u32 s82, 3
	s_cselect_b64 s[96:97], -1, 0
	s_sub_i32 s0, 3, s80
	s_mov_b32 s1, s16
	s_lshl_b64 s[0:1], s[0:1], 13
	v_readlane_b32 s9, v251, 59
	s_add_u32 s2, s9, s0
	v_readlane_b32 s10, v251, 61
	s_addc_u32 s3, s10, s1
	s_add_i32 s0, s79, 4
	s_mov_b32 s1, s16
	s_lshl_b64 s[0:1], s[0:1], 13
	v_writelane_b32 v249, s40, 10
	s_add_u32 s7, s92, s0
	s_mov_b32 s12, s16
	s_addc_u32 s8, s93, s1
	s_mov_b32 s1, s16
	v_writelane_b32 v249, s12, 11
	s_cmp_gt_u32 s82, 4
	s_cselect_b64 s[4:5], -1, 0
	v_writelane_b32 v249, s13, 12
	s_sub_i32 s0, 4, s80
	v_writelane_b32 v249, s14, 13
	s_lshl_b64 s[0:1], s[0:1], 13
	v_writelane_b32 v249, s15, 14
	s_add_u32 s9, s9, s0
	v_writelane_b32 v249, s16, 15
	s_addc_u32 s10, s10, s1
	s_add_i32 s0, s79, 5
	v_writelane_b32 v249, s17, 16
	s_mov_b32 s1, s16
	v_writelane_b32 v249, s18, 17
	s_lshl_b64 s[0:1], s[0:1], 13
	v_writelane_b32 v249, s19, 18
	s_add_u32 s0, s92, s0
	v_writelane_b32 v249, s20, 19
	s_addc_u32 s1, s93, s1
	s_sub_i32 s11, 30, s6
	v_writelane_b32 v249, s21, 20
	s_cmp_gt_i32 s80, 3
	v_writelane_b32 v249, s22, 21
	s_cselect_b32 s2, s7, s2
	v_writelane_b32 v249, s23, 22
	s_cselect_b32 s3, s8, s3
	s_add_u32 s2, s2, s90
	v_writelane_b32 v249, s24, 23
	s_addc_u32 s3, s3, s91
	v_writelane_b32 v249, s25, 24
	s_cmp_gt_i32 s80, 4
	v_writelane_b32 v249, s26, 25
	s_cselect_b32 s0, s0, s9
	v_writelane_b32 v249, s27, 26
	s_cselect_b32 s1, s1, s10
	s_add_u32 s12, s0, s90
	s_addc_u32 s13, s1, s91
	v_cmp_eq_u32_e32 vcc, 0, v198
	v_cmp_eq_u32_e64 s[0:1], s78, v198
	s_or_b64 s[0:1], vcc, s[0:1]
	v_cmp_eq_u32_e32 vcc, s11, v198
	s_or_b64 s[8:9], s[0:1], vcc
	v_readlane_b32 s0, v250, 44
	v_and_b32_e32 v4, 0x3fffffe0, v68
	v_lshl_add_u64 v[186:187], s[2:3], 0, v[184:185]
	v_lshl_add_u32 v206, v68, 2, s0
	v_lshl_add_u32 v207, v4, 2, s0
	s_mov_b64 s[0:1], 0x800000
	v_lshl_add_u64 v[190:191], s[12:13], 0, v[184:185]
	v_sub_u32_e32 v208, v71, v69
	v_lshl_add_u64 v[188:189], v[186:187], 0, s[0:1]
	v_lshl_add_u64 v[192:193], v[190:191], 0, s[0:1]
	v_mul_lo_u32 v3, v3, s64
	v_lshlrev_b32_e32 v4, 2, v198
	v_readlane_b32 s0, v250, 47
	v_lshlrev_b32_e32 v50, 2, v71
	v_mov_b32_e32 v16, v2
	v_add3_u32 v209, s0, v3, v4
	v_cmp_gt_i32_e64 s[0:1], 1, v208
	v_mov_b32_e32 v17, v2
	s_sub_i32 s83, s80, s6
	v_writelane_b32 v249, s0, 27
	v_mov_b32_e32 v3, v2
	v_mov_b32_e32 v4, v2
	v_writelane_b32 v249, s1, 28
	v_cmp_gt_i32_e64 s[0:1], 0, v208
	v_mov_b32_e32 v5, v2
	v_mov_b32_e32 v6, v2
	v_writelane_b32 v249, s0, 29
	v_mov_b32_e32 v7, v2
	v_mov_b32_e32 v8, v2
	v_writelane_b32 v249, s1, 30
	v_cmp_gt_i32_e64 s[0:1], 33, v208
	v_mov_b32_e32 v9, v2
	v_mov_b32_e32 v10, v2
	v_writelane_b32 v249, s0, 31
	v_mov_b32_e32 v11, v2
	v_mov_b32_e32 v12, v2
	v_writelane_b32 v249, s1, 32
	v_cmp_gt_i32_e64 s[0:1], 32, v208
	v_mov_b32_e32 v13, v2
	v_mov_b32_e32 v14, v2
	v_writelane_b32 v249, s0, 33
	v_mov_b32_e32 v15, v2
	v_add_u32_e32 v50, 0, v50
	v_writelane_b32 v249, s1, 34
	v_cmp_gt_i32_e64 s[0:1], 3, v208
	v_mov_b64_e32 v[96:97], v[16:17]
	v_mov_b64_e32 v[112:113], v[16:17]
	v_writelane_b32 v249, s0, 35
	s_add_i32 s83, s83, 32
	v_cmp_lt_u32_e64 s[6:7], s78, v198
	v_writelane_b32 v249, s1, 36
	v_cmp_gt_i32_e64 s[0:1], 2, v208
	v_mov_b32_e32 v211, 0
	v_cmp_eq_u32_e64 s[10:11], 0, v68
	v_writelane_b32 v249, s0, 37
	v_cmp_ne_u32_e64 s[12:13], 0, v198
	v_cmp_lt_u32_e64 s[14:15], 1, v198
	v_writelane_b32 v249, s1, 38
	v_cmp_gt_i32_e64 s[0:1], 35, v208
	v_cmp_lt_u32_e64 s[16:17], 2, v198
	v_cmp_lt_u32_e64 s[18:19], 3, v198
	v_writelane_b32 v249, s0, 39
	v_cmp_lt_u32_e64 s[20:21], 4, v198
	v_cmp_lt_u32_e64 s[22:23], 5, v198
	v_writelane_b32 v249, s1, 40
	v_cmp_gt_i32_e64 s[0:1], 34, v208
	v_cmp_lt_u32_e64 s[24:25], 6, v198
	v_cmp_lt_u32_e64 s[26:27], 7, v198
	v_writelane_b32 v249, s0, 41
	v_cmp_lt_u32_e64 s[28:29], 8, v198
	v_cmp_lt_u32_e64 s[30:31], 9, v198
	v_writelane_b32 v249, s1, 42
	v_cmp_gt_i32_e64 s[0:1], 9, v208
	v_cmp_lt_u32_e64 s[34:35], 10, v198
	v_cmp_lt_u32_e64 s[36:37], 11, v198
	v_writelane_b32 v249, s0, 43
	v_cmp_lt_u32_e64 s[38:39], 12, v198
	v_cmp_lt_u32_e64 s[40:41], 13, v198
	v_writelane_b32 v249, s1, 44
	v_cmp_gt_i32_e64 s[0:1], 8, v208
	v_cmp_lt_u32_e64 s[42:43], 14, v198
	v_cmp_lt_u32_e64 s[44:45], 15, v198
	v_writelane_b32 v249, s0, 45
	v_cmp_lt_u32_e64 s[46:47], 16, v198
	v_cmp_lt_u32_e64 s[48:49], 17, v198
	v_writelane_b32 v249, s1, 46
	v_cmp_gt_i32_e64 s[0:1], 41, v208
	v_cmp_lt_u32_e64 s[50:51], 18, v198
	v_cmp_lt_u32_e64 s[52:53], 19, v198
	v_writelane_b32 v249, s0, 47
	v_cmp_lt_u32_e64 s[54:55], 20, v198
	v_cmp_lt_u32_e64 s[56:57], 21, v198
	v_writelane_b32 v249, s1, 48
	v_cmp_gt_i32_e64 s[0:1], 40, v208
	v_cmp_lt_u32_e64 s[58:59], 22, v198
	v_cmp_lt_u32_e64 s[60:61], 23, v198
	v_writelane_b32 v249, s0, 49
	v_cmp_lt_u32_e64 s[62:63], 24, v198
	s_mov_b32 s2, 0
	v_writelane_b32 v249, s1, 50
	v_cmp_gt_i32_e64 s[0:1], 11, v208
	v_mov_b32_e32 v214, 0
	v_add_u32_e32 v210, 0x20400, v50
	v_writelane_b32 v249, s0, 51
	v_mov_b32_e32 v114, 0
	v_mov_b64_e32 v[94:95], v[14:15]
	v_writelane_b32 v249, s1, 52
	v_cmp_gt_i32_e64 s[0:1], 10, v208
	v_mov_b64_e32 v[92:93], v[12:13]
	v_mov_b64_e32 v[90:91], v[10:11]
	v_writelane_b32 v249, s0, 53
	v_mov_b64_e32 v[88:89], v[8:9]
	v_mov_b64_e32 v[86:87], v[6:7]
	v_writelane_b32 v249, s1, 54
	v_cmp_gt_i32_e64 s[0:1], 43, v208
	v_mov_b64_e32 v[84:85], v[4:5]
	v_mov_b64_e32 v[82:83], v[2:3]
	v_writelane_b32 v249, s0, 55
	v_mov_b64_e32 v[110:111], v[14:15]
	v_mov_b64_e32 v[108:109], v[12:13]
	v_writelane_b32 v249, s1, 56
	v_cmp_gt_i32_e64 s[0:1], 42, v208
	v_mov_b64_e32 v[106:107], v[10:11]
	v_mov_b64_e32 v[104:105], v[8:9]
	v_writelane_b32 v249, s0, 57
	v_mov_b64_e32 v[102:103], v[6:7]
	v_mov_b64_e32 v[100:101], v[4:5]
	v_writelane_b32 v249, s1, 58
	v_cmp_gt_i32_e64 s[0:1], 17, v208
	v_mov_b64_e32 v[98:99], v[2:3]
	v_cmp_lt_u32_e64 s[64:65], 25, v198
	v_writelane_b32 v249, s0, 59
	v_cmp_lt_u32_e64 s[66:67], 26, v198
	v_cmp_lt_u32_e64 s[68:69], 27, v198
	v_writelane_b32 v249, s1, 60
	v_cmp_gt_i32_e64 s[0:1], 16, v208
	v_cmp_lt_u32_e64 s[70:71], 28, v198
	v_cmp_lt_u32_e64 s[72:73], 29, v198
	v_writelane_b32 v249, s0, 61
	v_cmp_eq_u32_e64 s[74:75], 31, v198
	s_nop 0
	v_writelane_b32 v249, s1, 62
	v_cmp_gt_i32_e64 s[0:1], 49, v208
	s_nop 1
	v_writelane_b32 v249, s0, 63
	s_nop 1
	v_writelane_b32 v248, s1, 0
	v_cmp_gt_i32_e64 s[0:1], 48, v208
	s_nop 1
	v_writelane_b32 v248, s0, 1
	s_nop 1
	v_writelane_b32 v248, s1, 2
	v_cmp_gt_i32_e64 s[0:1], 19, v208
	s_nop 1
	v_writelane_b32 v248, s0, 3
	s_nop 1
	v_writelane_b32 v248, s1, 4
	v_cmp_gt_i32_e64 s[0:1], 18, v208
	s_nop 1
	v_writelane_b32 v248, s0, 5
	s_nop 1
	v_writelane_b32 v248, s1, 6
	v_cmp_gt_i32_e64 s[0:1], 51, v208
	s_nop 1
	v_writelane_b32 v248, s0, 7
	s_nop 1
	v_writelane_b32 v248, s1, 8
	v_cmp_gt_i32_e64 s[0:1], 50, v208
	s_nop 1
	v_writelane_b32 v248, s0, 9
	s_nop 1
	v_writelane_b32 v248, s1, 10
	v_cmp_gt_i32_e64 s[0:1], 25, v208
	s_nop 1
	v_writelane_b32 v248, s0, 11
	s_nop 1
	v_writelane_b32 v248, s1, 12
	v_cmp_gt_i32_e64 s[0:1], 24, v208
	s_nop 1
	v_writelane_b32 v248, s0, 13
	s_nop 1
	v_writelane_b32 v248, s1, 14
	v_cmp_gt_i32_e64 s[0:1], 57, v208
	s_nop 1
	v_writelane_b32 v248, s0, 15
	s_nop 1
	v_writelane_b32 v248, s1, 16
	v_cmp_gt_i32_e64 s[0:1], 56, v208
	s_nop 1
	v_writelane_b32 v248, s0, 17
	s_nop 1
	v_writelane_b32 v248, s1, 18
	v_cmp_gt_i32_e64 s[0:1], 27, v208
	s_nop 1
	v_writelane_b32 v248, s0, 19
	s_nop 1
	v_writelane_b32 v248, s1, 20
	v_cmp_gt_i32_e64 s[0:1], 26, v208
	s_nop 1
	v_writelane_b32 v248, s0, 21
	s_nop 1
	v_writelane_b32 v248, s1, 22
	v_cmp_gt_i32_e64 s[0:1], 59, v208
	s_nop 1
	v_writelane_b32 v248, s0, 23
	s_nop 1
	v_writelane_b32 v248, s1, 24
	v_cmp_gt_i32_e64 s[0:1], 58, v208
	s_nop 1
	v_writelane_b32 v248, s0, 25
	s_nop 1
	v_writelane_b32 v248, s1, 26
	v_mov_b64_e32 v[50:51], 0
	v_mov_b64_e32 v[52:53], 0
	v_mov_b64_e32 v[54:55], 0
	v_mov_b64_e32 v[56:57], 0
	v_mov_b64_e32 v[58:59], 0
	v_mov_b64_e32 v[60:61], 0
	v_mov_b64_e32 v[62:63], 0
	v_mov_b64_e32 v[64:65], 0
	v_mov_b64_e32 v[66:67], 0
	v_mov_b64_e32 v[68:69], 0
	v_mov_b64_e32 v[70:71], 0
	v_mov_b64_e32 v[72:73], 0
	v_mov_b64_e32 v[74:75], 0
	v_mov_b64_e32 v[76:77], 0
	v_mov_b64_e32 v[78:79], 0
	v_mov_b64_e32 v[80:81], 0

.LBB0_599:
	s_cmp_eq_u32 s2, s81
	s_cselect_b64 s[84:85], -1, 0
	s_cmp_lg_u32 s2, s81
	s_cbranch_scc1 .LBB0_601
	v_mov_b32_e32 v3, v114
	s_nop 1
	v_permlane32_swap_b32_e32 v114, v3
	v_add_f32_e32 v3, v114, v3
	v_div_scale_f32 v4, s[0:1], v3, v3, 1.0
	v_rcp_f32_e32 v5, v4
	s_waitcnt lgkmcnt(0)
	ds_read_b32 v211, v210
	v_mov_b32_e32 v16, v2
	v_mov_b32_e32 v17, v2
	v_fma_f32 v6, -v4, v5, 1.0
	v_fmac_f32_e32 v5, v6, v5
	v_div_scale_f32 v6, vcc, 1.0, v3, 1.0
	v_mul_f32_e32 v7, v6, v5
	v_fma_f32 v8, -v4, v7, v6
	v_fmac_f32_e32 v7, v8, v5
	v_fma_f32 v4, -v4, v7, v6
	v_div_fmas_f32 v4, v4, v5, v7
	v_div_fixup_f32 v4, v4, v3, 1.0
	v_cmp_lt_f32_e32 vcc, 0, v3
	v_mov_b32_e32 v6, v2
	v_mov_b32_e32 v7, v2
	v_cndmask_b32_e32 v3, 0, v4, vcc
	v_mul_f32_e32 v4, v200, v3
	v_pk_fma_f32 v[48:49], v[80:81], v[4:5], v[48:49] op_sel_hi:[1,0,1]
	v_pk_fma_f32 v[46:47], v[78:79], v[4:5], v[46:47] op_sel_hi:[1,0,1]
	v_pk_fma_f32 v[44:45], v[76:77], v[4:5], v[44:45] op_sel_hi:[1,0,1]
	v_pk_fma_f32 v[42:43], v[74:75], v[4:5], v[42:43] op_sel_hi:[1,0,1]
	v_pk_fma_f32 v[40:41], v[72:73], v[4:5], v[40:41] op_sel_hi:[1,0,1]
	v_pk_fma_f32 v[38:39], v[70:71], v[4:5], v[38:39] op_sel_hi:[1,0,1]
	v_pk_fma_f32 v[36:37], v[68:69], v[4:5], v[36:37] op_sel_hi:[1,0,1]
	v_pk_fma_f32 v[34:35], v[66:67], v[4:5], v[34:35] op_sel_hi:[1,0,1]
	v_pk_fma_f32 v[32:33], v[64:65], v[4:5], v[32:33] op_sel_hi:[1,0,1]
	v_pk_fma_f32 v[30:31], v[62:63], v[4:5], v[30:31] op_sel_hi:[1,0,1]
	v_pk_fma_f32 v[28:29], v[60:61], v[4:5], v[28:29] op_sel_hi:[1,0,1]
	v_pk_fma_f32 v[26:27], v[58:59], v[4:5], v[26:27] op_sel_hi:[1,0,1]
	v_pk_fma_f32 v[24:25], v[56:57], v[4:5], v[24:25] op_sel_hi:[1,0,1]
	v_pk_fma_f32 v[22:23], v[54:55], v[4:5], v[22:23] op_sel_hi:[1,0,1]
	v_pk_fma_f32 v[20:21], v[52:53], v[4:5], v[20:21] op_sel_hi:[1,0,1]
	v_pk_fma_f32 v[18:19], v[50:51], v[4:5], v[18:19] op_sel_hi:[1,0,1]
	v_mov_b32_e32 v3, v2
	v_mov_b32_e32 v4, v2
	v_mov_b32_e32 v5, v2
	v_mov_b32_e32 v8, v2
	v_mov_b32_e32 v9, v2
	v_mov_b32_e32 v10, v2
	v_mov_b32_e32 v11, v2
	v_mov_b32_e32 v12, v2
	v_mov_b32_e32 v13, v2
	v_mov_b32_e32 v14, v2
	v_mov_b32_e32 v15, v2
	v_mov_b64_e32 v[64:65], v[16:17]
	v_mov_b64_e32 v[80:81], v[16:17]
	v_mov_b32_e32 v213, 0
	v_mov_b64_e32 v[62:63], v[14:15]
	v_mov_b64_e32 v[60:61], v[12:13]
	v_mov_b64_e32 v[58:59], v[10:11]
	v_mov_b64_e32 v[56:57], v[8:9]
	v_mov_b64_e32 v[54:55], v[6:7]
	v_mov_b64_e32 v[52:53], v[4:5]
	v_mov_b64_e32 v[50:51], v[2:3]
	v_mov_b64_e32 v[78:79], v[14:15]
	v_mov_b64_e32 v[76:77], v[12:13]
	v_mov_b64_e32 v[74:75], v[10:11]
	v_mov_b64_e32 v[72:73], v[8:9]
	v_mov_b64_e32 v[70:71], v[6:7]
	v_mov_b64_e32 v[68:69], v[4:5]
	v_mov_b64_e32 v[66:67], v[2:3]
	v_mov_b32_e32 v3, 0
	s_branch .LBB0_602
.LBB0_601:
	v_mov_b32_e32 v213, v114
	v_mov_b32_e32 v3, v214
.LBB0_602:
	s_add_i32 s0, s2, 2
	s_mul_hi_u32 s1, s0, 0xaaaaaaab
	s_lshr_b32 s1, s1, 2
	s_mul_i32 s1, s1, 6
	s_sub_i32 s0, s0, s1
	s_lshl_b32 s0, s0, 14
	s_add_i32 s3, s0, 0
	s_cmp_gt_u32 s2, s80
	s_mov_b64 s[0:1], -1
	s_cbranch_scc1 .LBB0_617
	s_add_i32 s76, s2, s79
	s_cmp_eq_u32 s78, s76
	s_cselect_b64 s[0:1], -1, 0
	s_and_b64 vcc, s[94:95], s[86:87]
	s_or_b64 vcc, s[0:1], vcc
	s_mov_b64 s[0:1], -1
	s_and_b64 vcc, exec, vcc
	s_cbranch_vccnz .LBB0_607
	v_add3_u32 v16, s3, v203, v202
	ds_read_b128 v[4:7], v16
	ds_read_b128 v[8:11], v16 offset:512
	ds_read_b128 v[12:15], v16 offset:2048
	ds_read_b128 v[82:85], v16 offset:2560
	ds_read_b128 v[86:89], v16 offset:4096
	ds_read_b128 v[90:93], v16 offset:4608
	ds_read_b128 v[94:97], v16 offset:6144
	ds_read_b128 v[98:101], v16 offset:6656
	v_xor_b32_e32 v114, 0x80000000, v3
	v_mov_b32_e32 v115, v114
	v_mov_b32_e32 v116, v114
	v_mov_b32_e32 v117, v114
	v_mov_b32_e32 v118, v114
	v_mov_b32_e32 v119, v114
	v_mov_b32_e32 v120, v114
	v_mov_b32_e32 v121, v114
	v_mov_b32_e32 v122, v114
	v_mov_b32_e32 v123, v114
	v_mov_b32_e32 v124, v114
	v_mov_b32_e32 v125, v114
	v_mov_b32_e32 v126, v114
	v_mov_b32_e32 v127, v114
	v_mov_b32_e32 v128, v114
	v_mov_b32_e32 v129, v114
	s_waitcnt lgkmcnt(7)
	s_nop 0
	v_mfma_f32_32x32x16_bf16 v[130:145], v[4:7], v[158:161], v[114:129]
	v_add_u32_e32 v4, s3, v204
	v_add3_u32 v6, v4, v201, v205
	s_waitcnt lgkmcnt(6)
	v_mfma_f32_32x32x16_bf16 v[114:129], v[8:11], v[158:161], v[114:129]
	s_waitcnt lgkmcnt(5)
	v_mfma_f32_32x32x16_bf16 v[130:145], v[12:15], v[154:157], v[130:145]
	ds_read_b64_tr_b16 v[178:179], v6 offset:8192
	ds_read_b64_tr_b16 v[180:181], v6 offset:8704
	ds_read_b64_tr_b16 v[174:175], v6 offset:12288
	ds_read_b64_tr_b16 v[176:177], v6 offset:12800
	ds_read_b64_tr_b16 v[170:171], v6 offset:9216
	ds_read_b64_tr_b16 v[172:173], v6 offset:9728
	ds_read_b64_tr_b16 v[166:167], v6 offset:13312
	ds_read_b64_tr_b16 v[168:169], v6 offset:13824
	ds_read_b64_tr_b16 v[162:163], v6 offset:10240
	ds_read_b64_tr_b16 v[164:165], v6 offset:10752
	ds_read_b64_tr_b16 v[12:13], v6 offset:14336
	ds_read_b64_tr_b16 v[14:15], v6 offset:14848
	ds_read_b64_tr_b16 v[8:9], v6 offset:11264
	ds_read_b64_tr_b16 v[10:11], v6 offset:11776
	ds_read_b64_tr_b16 v[4:5], v6 offset:15360
	ds_read_b64_tr_b16 v[6:7], v6 offset:15872
	s_waitcnt lgkmcnt(14)
	v_mfma_f32_32x32x16_bf16 v[114:129], v[82:85], v[154:157], v[114:129]
	v_mfma_f32_32x32x16_bf16 v[130:145], v[86:89], v[150:153], v[130:145]
	v_mfma_f32_32x32x16_bf16 v[114:129], v[90:93], v[150:153], v[114:129]
	v_mfma_f32_32x32x16_bf16 v[130:145], v[94:97], v[146:149], v[130:145]
	v_mfma_f32_32x32x16_bf16 v[114:129], v[98:101], v[146:149], v[114:129]
	s_nop 10
	v_max_f32_e32 v16, v131, v131
	v_max_f32_e32 v17, v130, v130
	v_max_f32_e32 v16, v17, v16
	v_max3_f32 v17, v132, v133, v115
	v_max3_f32 v16, v16, v114, v116
	v_max3_f32 v16, v16, v117, v134
	v_max3_f32 v17, v17, v136, v137
	v_max3_f32 v16, v16, v135, v118
	v_max3_f32 v17, v17, v120, v121
	v_max3_f32 v16, v16, v119, v138
	v_max3_f32 v17, v17, v140, v141
	v_max3_f32 v16, v16, v139, v122
	v_max3_f32 v17, v17, v124, v125
	v_max3_f32 v16, v16, v123, v142
	v_max3_f32 v17, v17, v144, v145
	v_max3_f32 v16, v16, v143, v126
	v_max3_f32 v17, v17, v128, v129
	v_max3_f32 v16, v16, v127, v17
	v_mov_b32_e32 v17, v16
	s_nop 1
	v_permlane32_swap_b32_e32 v16, v17
	v_max_f32_e32 v17, v17, v17
	v_max_f32_e32 v16, v16, v16
	v_max_f32_e32 v17, v16, v17
	s_mov_b32 s0, 0x41000000
	v_cmp_lt_f32_e32 vcc, s0, v17
	s_cmp_lg_u64 vcc, 0
	s_cselect_b64 s[0:1], -1, 0
	s_or_b64 s[0:1], s[86:87], s[0:1]
	s_and_b64 vcc, exec, s[0:1]
	v_mov_b32_e32 v16, v213
	v_mov_b32_e32 v214, v3
	s_cbranch_vccz .LBB0_606
	v_cndmask_b32_e64 v16, 0, v197, s[86:87]
	v_max_f32_e32 v17, v17, v17
	v_max_f32_e32 v16, v17, v16
	v_exp_f32_e64 v216, -v16
	v_add_f32_e32 v214, v3, v16
	v_pk_add_f32 v[130:131], v[130:131], v[16:17] op_sel_hi:[1,0] neg_lo:[0,1] neg_hi:[0,1]
	v_pk_add_f32 v[114:115], v[114:115], v[16:17] op_sel_hi:[1,0] neg_lo:[0,1] neg_hi:[0,1]
	v_pk_add_f32 v[132:133], v[132:133], v[16:17] op_sel_hi:[1,0] neg_lo:[0,1] neg_hi:[0,1]
	v_pk_add_f32 v[116:117], v[116:117], v[16:17] op_sel_hi:[1,0] neg_lo:[0,1] neg_hi:[0,1]
	v_pk_add_f32 v[134:135], v[134:135], v[16:17] op_sel_hi:[1,0] neg_lo:[0,1] neg_hi:[0,1]
	v_pk_add_f32 v[118:119], v[118:119], v[16:17] op_sel_hi:[1,0] neg_lo:[0,1] neg_hi:[0,1]
	v_pk_add_f32 v[136:137], v[136:137], v[16:17] op_sel_hi:[1,0] neg_lo:[0,1] neg_hi:[0,1]
	v_pk_add_f32 v[120:121], v[120:121], v[16:17] op_sel_hi:[1,0] neg_lo:[0,1] neg_hi:[0,1]
	v_pk_add_f32 v[138:139], v[138:139], v[16:17] op_sel_hi:[1,0] neg_lo:[0,1] neg_hi:[0,1]
	v_pk_add_f32 v[122:123], v[122:123], v[16:17] op_sel_hi:[1,0] neg_lo:[0,1] neg_hi:[0,1]
	v_pk_add_f32 v[140:141], v[140:141], v[16:17] op_sel_hi:[1,0] neg_lo:[0,1] neg_hi:[0,1]
	v_pk_add_f32 v[124:125], v[124:125], v[16:17] op_sel_hi:[1,0] neg_lo:[0,1] neg_hi:[0,1]
	v_pk_add_f32 v[142:143], v[142:143], v[16:17] op_sel_hi:[1,0] neg_lo:[0,1] neg_hi:[0,1]
	v_pk_add_f32 v[126:127], v[126:127], v[16:17] op_sel_hi:[1,0] neg_lo:[0,1] neg_hi:[0,1]
	v_pk_add_f32 v[144:145], v[144:145], v[16:17] op_sel_hi:[1,0] neg_lo:[0,1] neg_hi:[0,1]
	v_pk_add_f32 v[128:129], v[128:129], v[16:17] op_sel_hi:[1,0] neg_lo:[0,1] neg_hi:[0,1]
	v_pk_mul_f32 v[80:81], v[80:81], v[216:217] op_sel_hi:[1,0]
	v_pk_mul_f32 v[78:79], v[78:79], v[216:217] op_sel_hi:[1,0]
	v_pk_mul_f32 v[76:77], v[76:77], v[216:217] op_sel_hi:[1,0]
	v_pk_mul_f32 v[74:75], v[74:75], v[216:217] op_sel_hi:[1,0]
	v_pk_mul_f32 v[72:73], v[72:73], v[216:217] op_sel_hi:[1,0]
	v_pk_mul_f32 v[70:71], v[70:71], v[216:217] op_sel_hi:[1,0]
	v_pk_mul_f32 v[68:69], v[68:69], v[216:217] op_sel_hi:[1,0]
	v_pk_mul_f32 v[66:67], v[66:67], v[216:217] op_sel_hi:[1,0]
	v_pk_mul_f32 v[64:65], v[64:65], v[216:217] op_sel_hi:[1,0]
	v_pk_mul_f32 v[62:63], v[62:63], v[216:217] op_sel_hi:[1,0]
	v_pk_mul_f32 v[60:61], v[60:61], v[216:217] op_sel_hi:[1,0]
	v_pk_mul_f32 v[58:59], v[58:59], v[216:217] op_sel_hi:[1,0]
	v_pk_mul_f32 v[56:57], v[56:57], v[216:217] op_sel_hi:[1,0]
	v_pk_mul_f32 v[54:55], v[54:55], v[216:217] op_sel_hi:[1,0]
	v_pk_mul_f32 v[52:53], v[52:53], v[216:217] op_sel_hi:[1,0]
	v_pk_mul_f32 v[50:51], v[50:51], v[216:217] op_sel_hi:[1,0]
	v_mul_f32_e32 v16, v213, v216
.LBB0_606:
	v_exp_f32_e32 v216, v130
	v_exp_f32_e32 v218, v131
	v_exp_f32_e32 v220, v132
	v_exp_f32_e32 v222, v133
	v_exp_f32_e32 v134, v134
	v_exp_f32_e32 v224, v135
	v_exp_f32_e32 v136, v136
	v_exp_f32_e32 v226, v137
	v_exp_f32_e32 v217, v114
	v_cvt_pk_bf16_f32 v130, v216, v218
	v_cvt_pk_bf16_f32 v131, v220, v222
	v_cvt_pk_bf16_f32 v132, v134, v224
	v_cvt_pk_bf16_f32 v133, v136, v226
	v_exp_f32_e32 v219, v115
	v_pk_add_f32 v[114:115], v[216:217], 0 op_sel_hi:[1,0]
	v_mfma_f32_32x32x16_bf16 v[66:81], v[178:181], v[130:133], v[66:81]
	v_exp_f32_e32 v221, v116
	v_exp_f32_e32 v138, v138
	v_exp_f32_e32 v180, v139
	v_exp_f32_e32 v140, v140
	v_exp_f32_e32 v216, v141
	v_exp_f32_e32 v142, v142
	v_pk_add_f32 v[114:115], v[218:219], v[114:115]
	s_waitcnt lgkmcnt(12)
	v_mfma_f32_32x32x16_bf16 v[50:65], v[174:177], v[130:133], v[50:65]
	v_exp_f32_e32 v130, v143
	v_exp_f32_e32 v132, v144
	v_exp_f32_e32 v144, v145
	v_pk_add_f32 v[178:179], v[220:221], v[114:115]
	v_exp_f32_e32 v223, v117
	v_cvt_pk_bf16_f32 v114, v138, v180
	v_cvt_pk_bf16_f32 v115, v140, v216
	v_cvt_pk_bf16_f32 v116, v142, v130
	v_cvt_pk_bf16_f32 v117, v132, v144
	v_exp_f32_e32 v135, v118
	v_exp_f32_e32 v225, v119
	s_waitcnt lgkmcnt(10)
	v_mfma_f32_32x32x16_bf16 v[66:81], v[170:173], v[114:117], v[66:81]
	v_exp_f32_e32 v137, v120
	v_exp_f32_e32 v227, v121
	v_pk_add_f32 v[118:119], v[222:223], v[178:179]
	v_exp_f32_e32 v139, v122
	v_pk_add_f32 v[118:119], v[134:135], v[118:119]
	v_exp_f32_e32 v181, v123
	v_pk_add_f32 v[118:119], v[224:225], v[118:119]
	s_waitcnt lgkmcnt(8)
	v_mfma_f32_32x32x16_bf16 v[50:65], v[166:169], v[114:117], v[50:65]
	v_cvt_pk_bf16_f32 v114, v217, v219
	v_cvt_pk_bf16_f32 v115, v221, v223
	v_cvt_pk_bf16_f32 v116, v135, v225
	v_cvt_pk_bf16_f32 v117, v137, v227
	v_exp_f32_e32 v141, v124
	v_exp_f32_e32 v217, v125
	v_exp_f32_e32 v143, v126
	s_waitcnt lgkmcnt(6)
	v_mfma_f32_32x32x16_bf16 v[66:81], v[162:165], v[114:117], v[66:81]
	v_exp_f32_e32 v131, v127
	v_exp_f32_e32 v133, v128
	v_exp_f32_e32 v145, v129
	v_pk_add_f32 v[118:119], v[136:137], v[118:119]
	s_mov_b64 s[0:1], 0
	v_pk_add_f32 v[118:119], v[226:227], v[118:119]
	s_waitcnt lgkmcnt(4)
	v_mfma_f32_32x32x16_bf16 v[50:65], v[12:15], v[114:117], v[50:65]
	v_add_f32_e64 v118, v138, v118
	v_add_f32_e64 v119, v139, v119
	v_cvt_pk_bf16_f32 v12, v139, v181
	v_add_f32_e64 v118, v180, v118
	v_add_f32_e64 v119, v181, v119
	v_cvt_pk_bf16_f32 v13, v141, v217
	v_cvt_pk_bf16_f32 v14, v143, v131
	v_cvt_pk_bf16_f32 v15, v133, v145
	v_pk_add_f32 v[118:119], v[140:141], v[118:119]
	s_waitcnt lgkmcnt(2)
	v_mfma_f32_32x32x16_bf16 v[66:81], v[8:11], v[12:15], v[66:81]
	v_add_f32_e64 v8, v216, v118
	v_add_f32_e64 v9, v217, v119
	v_add_f32_e64 v8, v142, v8
	v_add_f32_e64 v9, v143, v9
	v_add_f32_e64 v8, v130, v8
	v_add_f32_e64 v9, v131, v9
	v_pk_add_f32 v[8:9], v[132:133], v[8:9]
	s_waitcnt lgkmcnt(0)
	v_mfma_f32_32x32x16_bf16 v[50:65], v[4:7], v[12:15], v[50:65]
	v_add_f32_e64 v8, v144, v8
	v_add_f32_e64 v9, v145, v9
	v_add_f32_e32 v8, v8, v9
	v_add_f32_e32 v114, v16, v8
.LBB0_607:
	s_and_b64 vcc, exec, s[0:1]
	s_cbranch_vccz .LBB0_616
	v_add3_u32 v16, s3, v203, v202
	ds_read_b128 v[4:7], v16
	ds_read_b128 v[8:11], v16 offset:512
	ds_read_b128 v[12:15], v16 offset:2048
	ds_read_b128 v[114:117], v16 offset:2560
	ds_read_b128 v[118:121], v16 offset:4096
	ds_read_b128 v[122:125], v16 offset:4608
	ds_read_b128 v[126:129], v16 offset:6144
	ds_read_b128 v[130:133], v16 offset:6656
	v_xor_b32_e32 v82, 0x80000000, v3
	s_sub_i32 s0, s78, s76
	v_mov_b32_e32 v83, v82
	v_mov_b32_e32 v84, v82
	v_mov_b32_e32 v85, v82
	v_mov_b32_e32 v86, v82
	v_mov_b32_e32 v87, v82
	v_mov_b32_e32 v88, v82
	v_mov_b32_e32 v89, v82
	v_mov_b32_e32 v90, v82
	v_mov_b32_e32 v91, v82
	v_mov_b32_e32 v92, v82
	v_mov_b32_e32 v93, v82
	v_mov_b32_e32 v94, v82
	v_mov_b32_e32 v95, v82
	v_mov_b32_e32 v96, v82
	v_mov_b32_e32 v97, v82
	s_waitcnt lgkmcnt(7)
	s_nop 0
	v_mfma_f32_32x32x16_bf16 v[98:113], v[4:7], v[158:161], v[82:97]
	v_add_u32_e32 v4, s3, v204
	v_add3_u32 v6, v4, v201, v205
	s_waitcnt lgkmcnt(6)
	v_mfma_f32_32x32x16_bf16 v[82:97], v[8:11], v[158:161], v[82:97]
	s_waitcnt lgkmcnt(5)
	v_mfma_f32_32x32x16_bf16 v[98:113], v[12:15], v[154:157], v[98:113]
	s_waitcnt lgkmcnt(4)
	v_mfma_f32_32x32x16_bf16 v[82:97], v[114:117], v[154:157], v[82:97]
	s_waitcnt lgkmcnt(3)
	v_mfma_f32_32x32x16_bf16 v[98:113], v[118:121], v[150:153], v[98:113]
	s_waitcnt lgkmcnt(2)
	v_mfma_f32_32x32x16_bf16 v[82:97], v[122:125], v[150:153], v[82:97]
	s_waitcnt lgkmcnt(1)
	v_mfma_f32_32x32x16_bf16 v[98:113], v[126:129], v[146:149], v[98:113]
	s_waitcnt lgkmcnt(0)
	v_mfma_f32_32x32x16_bf16 v[82:97], v[130:133], v[146:149], v[82:97]
	ds_read_b64_tr_b16 v[130:131], v6 offset:8192
	ds_read_b64_tr_b16 v[132:133], v6 offset:8704
	ds_read_b64_tr_b16 v[126:127], v6 offset:12288
	ds_read_b64_tr_b16 v[128:129], v6 offset:12800
	ds_read_b64_tr_b16 v[122:123], v6 offset:9216
	ds_read_b64_tr_b16 v[124:125], v6 offset:9728
	ds_read_b64_tr_b16 v[118:119], v6 offset:13312
	ds_read_b64_tr_b16 v[120:121], v6 offset:13824
	ds_read_b64_tr_b16 v[114:115], v6 offset:10240
	ds_read_b64_tr_b16 v[116:117], v6 offset:10752
	ds_read_b64_tr_b16 v[12:13], v6 offset:14336
	ds_read_b64_tr_b16 v[14:15], v6 offset:14848
	ds_read_b64_tr_b16 v[8:9], v6 offset:11264
	ds_read_b64_tr_b16 v[10:11], v6 offset:11776
	ds_read_b64_tr_b16 v[4:5], v6 offset:15360
	ds_read_b64_tr_b16 v[6:7], v6 offset:15872
	v_lshl_add_u32 v143, s0, 6, v208
	v_add_u32_e32 v16, -1, v143
	v_cmp_gt_u32_e32 vcc, s77, v16
	v_subrev_u32_e32 v16, 33, v143
	v_subrev_u32_e32 v17, 32, v143
	v_cndmask_b32_e32 v169, v195, v99, vcc
	v_cmp_gt_u32_e32 vcc, s77, v143
	s_mov_b32 s0, 0x41000000
	s_nop 0
	v_cndmask_b32_e32 v172, v195, v98, vcc
	v_cmp_gt_u32_e32 vcc, s77, v16
	v_add_u32_e32 v16, -3, v143
	s_nop 0
	v_cndmask_b32_e32 v171, v195, v83, vcc
	v_cmp_gt_u32_e32 vcc, s77, v17
	v_add_u32_e32 v17, -2, v143
	v_add_u32_e32 v83, -10, v143
	v_cndmask_b32_e32 v176, v195, v82, vcc
	v_cmp_gt_u32_e32 vcc, s77, v16
	v_subrev_u32_e32 v16, 35, v143
	v_add_u32_e32 v82, -11, v143
	v_cndmask_b32_e32 v170, v195, v101, vcc
	v_cmp_gt_u32_e32 vcc, s77, v17
	v_subrev_u32_e32 v17, 34, v143
	s_nop 0
	v_cndmask_b32_e32 v174, v195, v100, vcc
	v_cmp_gt_u32_e32 vcc, s77, v16
	v_add_u32_e32 v16, -9, v143
	s_nop 0
	v_cndmask_b32_e32 v135, v195, v85, vcc
	v_cmp_gt_u32_e32 vcc, s77, v17
	v_add_u32_e32 v17, -8, v143
	s_nop 0
	v_cndmask_b32_e32 v178, v195, v84, vcc
	v_cmp_gt_u32_e32 vcc, s77, v16
	v_subrev_u32_e32 v16, 41, v143
	s_nop 0
	v_cndmask_b32_e32 v173, v195, v103, vcc
	v_cmp_gt_u32_e32 vcc, s77, v17
	v_subrev_u32_e32 v17, 40, v143
	s_nop 0
	v_cndmask_b32_e32 v177, v195, v102, vcc
	v_cmp_gt_u32_e32 vcc, s77, v16
	s_nop 1
	v_cndmask_b32_e32 v16, v195, v87, vcc
	v_cmp_gt_u32_e32 vcc, s77, v17
	s_nop 1
	v_cndmask_b32_e32 v17, v195, v86, vcc
	v_cmp_gt_u32_e32 vcc, s77, v82
	v_subrev_u32_e32 v82, 43, v143
	s_nop 0
	v_cndmask_b32_e32 v175, v195, v105, vcc
	v_cmp_gt_u32_e32 vcc, s77, v83
	v_subrev_u32_e32 v83, 42, v143
	s_nop 0
	v_cndmask_b32_e32 v179, v195, v104, vcc
	v_cmp_gt_u32_e32 vcc, s77, v82
	v_subrev_u32_e32 v82, 17, v143
	s_nop 0
	v_cndmask_b32_e32 v134, v195, v89, vcc
	v_cmp_gt_u32_e32 vcc, s77, v83
	v_add_u32_e32 v83, -16, v143
	s_nop 0
	v_cndmask_b32_e32 v137, v195, v88, vcc
	v_cmp_gt_u32_e32 vcc, s77, v82
	v_subrev_u32_e32 v82, 49, v143
	s_nop 0
	v_cndmask_b32_e32 v145, v195, v107, vcc
	v_cmp_gt_u32_e32 vcc, s77, v83
	v_subrev_u32_e32 v83, 48, v143
	s_nop 0
	v_cndmask_b32_e32 v162, v195, v106, vcc
	v_cmp_gt_u32_e32 vcc, s77, v82
	v_subrev_u32_e32 v82, 19, v143
	s_nop 0
	v_cndmask_b32_e32 v138, v195, v91, vcc
	v_cmp_gt_u32_e32 vcc, s77, v83
	v_subrev_u32_e32 v83, 18, v143
	s_nop 0
	v_cndmask_b32_e32 v140, v195, v90, vcc
	v_cmp_gt_u32_e32 vcc, s77, v82
	v_subrev_u32_e32 v82, 51, v143
	s_nop 0
	v_cndmask_b32_e32 v163, v195, v109, vcc
	v_cmp_gt_u32_e32 vcc, s77, v83
	v_subrev_u32_e32 v83, 50, v143
	s_nop 0
	v_cndmask_b32_e32 v164, v195, v108, vcc
	v_cmp_gt_u32_e32 vcc, s77, v82
	v_subrev_u32_e32 v82, 25, v143
	s_nop 0
	v_cndmask_b32_e32 v136, v195, v93, vcc
	v_cmp_gt_u32_e32 vcc, s77, v83
	v_subrev_u32_e32 v83, 24, v143
	s_nop 0
	v_cndmask_b32_e32 v139, v195, v92, vcc
	v_cmp_gt_u32_e32 vcc, s77, v82
	v_subrev_u32_e32 v82, 57, v143
	s_nop 0
	v_cndmask_b32_e32 v165, v195, v111, vcc
	v_cmp_gt_u32_e32 vcc, s77, v83
	v_subrev_u32_e32 v83, 56, v143
	s_nop 0
	v_cndmask_b32_e32 v166, v195, v110, vcc
	v_cmp_gt_u32_e32 vcc, s77, v82
	v_subrev_u32_e32 v82, 27, v143
	s_nop 0
	v_cndmask_b32_e32 v141, v195, v95, vcc
	v_cmp_gt_u32_e32 vcc, s77, v83
	v_subrev_u32_e32 v83, 26, v143
	s_nop 0
	v_cndmask_b32_e32 v142, v195, v94, vcc
	v_cmp_gt_u32_e32 vcc, s77, v82
	v_subrev_u32_e32 v82, 59, v143
	s_nop 0
	v_cndmask_b32_e32 v167, v195, v113, vcc
	v_cmp_gt_u32_e32 vcc, s77, v83
	v_subrev_u32_e32 v83, 58, v143
	s_nop 0
	v_cndmask_b32_e32 v168, v195, v112, vcc
	v_cmp_gt_u32_e32 vcc, s77, v82
	v_max_f32_e32 v82, v169, v169
	s_nop 0
	v_cndmask_b32_e32 v143, v195, v97, vcc
	v_cmp_gt_u32_e32 vcc, s77, v83
	v_max_f32_e32 v83, v172, v172
	v_max_f32_e32 v82, v83, v82
	v_max3_f32 v83, v174, v170, v171
	v_max3_f32 v82, v82, v176, v178
	v_max3_f32 v82, v82, v135, v177
	v_max3_f32 v83, v83, v179, v175
	v_max3_f32 v82, v82, v173, v17
	v_max3_f32 v83, v83, v137, v134
	v_max3_f32 v82, v82, v16, v162
	v_max3_f32 v83, v83, v164, v163
	v_max3_f32 v82, v82, v145, v140
	v_max3_f32 v83, v83, v139, v136
	v_cndmask_b32_e32 v144, v195, v96, vcc
	v_max3_f32 v82, v82, v138, v166
	v_max3_f32 v83, v83, v168, v167
	v_max3_f32 v82, v82, v165, v142
	v_max3_f32 v83, v83, v144, v143
	v_max3_f32 v82, v82, v141, v83
	v_mov_b32_e32 v83, v82
	s_nop 1
	v_permlane32_swap_b32_e32 v82, v83
	v_max_f32_e32 v83, v83, v83
	v_max_f32_e32 v82, v82, v82
	v_max_f32_e32 v82, v82, v83
	v_cmp_lt_f32_e32 vcc, s0, v82
	s_cmp_eq_u64 vcc, 0
	s_cselect_b64 s[0:1], -1, 0
	s_xor_b64 vcc, s[86:87], -1
	s_and_b64 s[0:1], vcc, s[0:1]
	s_and_b64 vcc, exec, s[0:1]
	s_cbranch_vccnz .LBB0_614
	v_cndmask_b32_e64 v83, 0, v197, s[86:87]
	v_max_f32_e32 v82, v82, v82
	v_max_f32_e32 v82, v82, v83
	v_exp_f32_e64 v180, -v82
	v_add_f32_e32 v214, v3, v82
	v_sub_f32_e32 v172, v172, v82
	v_sub_f32_e32 v169, v169, v82
	v_sub_f32_e32 v174, v174, v82
	v_sub_f32_e32 v170, v170, v82
	v_sub_f32_e32 v177, v177, v82
	v_sub_f32_e32 v173, v173, v82
	v_sub_f32_e32 v179, v179, v82
	v_sub_f32_e32 v175, v175, v82
	v_sub_f32_e32 v162, v162, v82
	v_sub_f32_e32 v145, v145, v82
	v_sub_f32_e32 v164, v164, v82
	v_sub_f32_e32 v163, v163, v82
	v_sub_f32_e32 v166, v166, v82
	v_sub_f32_e32 v165, v165, v82
	v_sub_f32_e32 v168, v168, v82
	v_sub_f32_e32 v167, v167, v82
	v_sub_f32_e32 v176, v176, v82
	v_sub_f32_e32 v171, v171, v82
	v_sub_f32_e32 v178, v178, v82
	v_sub_f32_e32 v135, v135, v82
	v_sub_f32_e32 v17, v17, v82
	v_sub_f32_e32 v16, v16, v82
	v_sub_f32_e32 v137, v137, v82
	v_sub_f32_e32 v134, v134, v82
	v_sub_f32_e32 v140, v140, v82
	v_sub_f32_e32 v138, v138, v82
	v_sub_f32_e32 v139, v139, v82
	v_sub_f32_e32 v136, v136, v82
	v_sub_f32_e32 v142, v142, v82
	v_sub_f32_e32 v141, v141, v82
	v_sub_f32_e32 v144, v144, v82
	v_sub_f32_e32 v143, v143, v82
	v_pk_mul_f32 v[80:81], v[80:81], v[180:181] op_sel_hi:[1,0]
	v_pk_mul_f32 v[78:79], v[78:79], v[180:181] op_sel_hi:[1,0]
	v_pk_mul_f32 v[76:77], v[76:77], v[180:181] op_sel_hi:[1,0]
	v_pk_mul_f32 v[74:75], v[74:75], v[180:181] op_sel_hi:[1,0]
	v_pk_mul_f32 v[72:73], v[72:73], v[180:181] op_sel_hi:[1,0]
	v_pk_mul_f32 v[70:71], v[70:71], v[180:181] op_sel_hi:[1,0]
	v_pk_mul_f32 v[68:69], v[68:69], v[180:181] op_sel_hi:[1,0]
	v_pk_mul_f32 v[66:67], v[66:67], v[180:181] op_sel_hi:[1,0]
	v_pk_mul_f32 v[64:65], v[64:65], v[180:181] op_sel_hi:[1,0]
	v_pk_mul_f32 v[62:63], v[62:63], v[180:181] op_sel_hi:[1,0]
	v_pk_mul_f32 v[60:61], v[60:61], v[180:181] op_sel_hi:[1,0]
	v_pk_mul_f32 v[58:59], v[58:59], v[180:181] op_sel_hi:[1,0]
	v_pk_mul_f32 v[56:57], v[56:57], v[180:181] op_sel_hi:[1,0]
	v_pk_mul_f32 v[54:55], v[54:55], v[180:181] op_sel_hi:[1,0]
	v_pk_mul_f32 v[52:53], v[52:53], v[180:181] op_sel_hi:[1,0]
	v_pk_mul_f32 v[50:51], v[50:51], v[180:181] op_sel_hi:[1,0]
	v_mul_f32_e32 v180, v213, v180
	s_branch .LBB0_615

.LBB0_612:
	v_add_u32_e32 v4, 0, v3
	v_add_u32_e32 v5, 0x18000, v4
	v_add_u32_e32 v6, 0x1a100, v4
	v_add_u32_e32 v7, 0x1c200, v4
	v_add_u32_e32 v4, 0x1e300, v4
	ds_read_b32 v5, v5
	ds_read_b32 v6, v6
	ds_read_b32 v7, v7
	ds_read_b32 v4, v4
	s_waitcnt lgkmcnt(2)
	v_add_f32_e32 v5, v5, v6
	s_waitcnt lgkmcnt(1)
	v_add_f32_e32 v5, v5, v7
	s_waitcnt lgkmcnt(0)
	v_add_f32_e32 v4, v5, v4
	v_cndmask_b32_e64 v4, v4, v196, s[8:9]
	v_cndmask_b32_e64 v16, v4, v195, s[6:7]
	ds_write_b32 v206, v16
	s_waitcnt lgkmcnt(0)
	ds_read_b128 v[4:7], v207
	ds_read_b128 v[8:11], v207 offset:16
	ds_read_b128 v[12:15], v207 offset:32
	ds_read_b128 v[82:85], v207 offset:48
	s_waitcnt lgkmcnt(3)
	v_cmp_eq_f32_e64 s[84:85], v4, v16
	v_cmp_gt_f32_e32 vcc, v4, v16
	s_and_b64 s[0:1], s[84:85], s[12:13]
	s_or_b64 s[0:1], vcc, s[0:1]
	v_cmp_eq_f32_e64 s[84:85], v5, v16
	v_cndmask_b32_e64 v4, 0, 1, s[0:1]
	v_cmp_gt_f32_e32 vcc, v5, v16
	s_and_b64 s[0:1], s[84:85], s[14:15]
	s_or_b64 s[0:1], vcc, s[0:1]
	v_cmp_eq_f32_e64 s[84:85], v6, v16
	v_cndmask_b32_e64 v5, 0, 1, s[0:1]
	v_cmp_gt_f32_e32 vcc, v6, v16
	s_and_b64 s[0:1], s[84:85], s[16:17]
	s_or_b64 s[0:1], vcc, s[0:1]
	v_cmp_eq_f32_e64 s[84:85], v7, v16
	v_cndmask_b32_e64 v6, 0, 1, s[0:1]
	v_cmp_gt_f32_e32 vcc, v7, v16
	s_and_b64 s[0:1], s[84:85], s[18:19]
	s_or_b64 s[0:1], vcc, s[0:1]
	s_waitcnt lgkmcnt(2)
	v_cmp_eq_f32_e64 s[84:85], v8, v16
	v_add3_u32 v4, v4, v5, v6
	v_cndmask_b32_e64 v5, 0, 1, s[0:1]
	v_cmp_gt_f32_e32 vcc, v8, v16
	s_and_b64 s[0:1], s[84:85], s[20:21]
	s_or_b64 s[0:1], vcc, s[0:1]
	v_cmp_eq_f32_e64 s[84:85], v9, v16
	v_cndmask_b32_e64 v6, 0, 1, s[0:1]
	v_cmp_gt_f32_e32 vcc, v9, v16
	s_and_b64 s[0:1], s[84:85], s[22:23]
	s_or_b64 s[0:1], vcc, s[0:1]
	v_cmp_eq_f32_e64 s[84:85], v10, v16
	v_add3_u32 v4, v4, v5, v6
	v_cndmask_b32_e64 v5, 0, 1, s[0:1]
	v_cmp_gt_f32_e32 vcc, v10, v16
	s_and_b64 s[0:1], s[84:85], s[24:25]
	s_or_b64 s[0:1], vcc, s[0:1]
	v_cmp_eq_f32_e64 s[84:85], v11, v16
	v_cndmask_b32_e64 v6, 0, 1, s[0:1]
	v_cmp_gt_f32_e32 vcc, v11, v16
	s_and_b64 s[0:1], s[84:85], s[26:27]
	s_or_b64 s[0:1], vcc, s[0:1]
	s_waitcnt lgkmcnt(1)
	v_cmp_eq_f32_e64 s[84:85], v12, v16
	v_add3_u32 v4, v4, v5, v6
	v_cndmask_b32_e64 v5, 0, 1, s[0:1]
	v_cmp_gt_f32_e32 vcc, v12, v16
	s_and_b64 s[0:1], s[84:85], s[28:29]
	s_or_b64 s[0:1], vcc, s[0:1]
	v_cmp_eq_f32_e64 s[84:85], v13, v16
	v_cndmask_b32_e64 v6, 0, 1, s[0:1]
	v_cmp_gt_f32_e32 vcc, v13, v16
	s_and_b64 s[0:1], s[84:85], s[30:31]
	s_or_b64 s[0:1], vcc, s[0:1]
	v_cmp_eq_f32_e64 s[84:85], v14, v16
	v_add3_u32 v4, v4, v5, v6
	v_cndmask_b32_e64 v5, 0, 1, s[0:1]
	v_cmp_gt_f32_e32 vcc, v14, v16
	s_and_b64 s[0:1], s[84:85], s[34:35]
	s_or_b64 s[0:1], vcc, s[0:1]
	v_cmp_eq_f32_e64 s[84:85], v15, v16
	v_cndmask_b32_e64 v6, 0, 1, s[0:1]
	v_cmp_gt_f32_e32 vcc, v15, v16
	s_and_b64 s[0:1], s[84:85], s[36:37]
	s_or_b64 s[0:1], vcc, s[0:1]
	s_waitcnt lgkmcnt(0)
	v_cmp_eq_f32_e64 s[84:85], v82, v16
	v_add3_u32 v4, v4, v5, v6
	v_cndmask_b32_e64 v5, 0, 1, s[0:1]
	v_cmp_gt_f32_e32 vcc, v82, v16
	s_and_b64 s[0:1], s[84:85], s[38:39]
	s_or_b64 s[0:1], vcc, s[0:1]
	v_cmp_eq_f32_e64 s[84:85], v83, v16
	v_cndmask_b32_e64 v6, 0, 1, s[0:1]
	v_cmp_gt_f32_e32 vcc, v83, v16
	s_and_b64 s[0:1], s[84:85], s[40:41]
	s_or_b64 s[0:1], vcc, s[0:1]
	v_cmp_eq_f32_e64 s[84:85], v84, v16
	v_add3_u32 v4, v4, v5, v6
	v_cndmask_b32_e64 v5, 0, 1, s[0:1]
	v_cmp_gt_f32_e32 vcc, v84, v16
	s_and_b64 s[0:1], s[84:85], s[42:43]
	s_or_b64 s[0:1], vcc, s[0:1]
	v_cndmask_b32_e64 v6, 0, 1, s[0:1]
	v_add3_u32 v12, v4, v5, v6
	ds_read_b128 v[4:7], v207 offset:64
	ds_read_b128 v[8:11], v207 offset:80
	v_cmp_eq_f32_e64 s[84:85], v85, v16
	v_cmp_gt_f32_e32 vcc, v85, v16
	s_and_b64 s[0:1], s[84:85], s[44:45]
	s_or_b64 s[0:1], vcc, s[0:1]
	s_waitcnt lgkmcnt(1)
	v_cmp_eq_f32_e64 s[84:85], v4, v16
	v_cndmask_b32_e64 v13, 0, 1, s[0:1]
	v_cmp_gt_f32_e32 vcc, v4, v16
	s_and_b64 s[0:1], s[84:85], s[46:47]
	s_or_b64 s[0:1], vcc, s[0:1]
	v_cmp_eq_f32_e64 s[84:85], v5, v16
	v_cndmask_b32_e64 v4, 0, 1, s[0:1]
	v_cmp_gt_f32_e32 vcc, v5, v16
	s_and_b64 s[0:1], s[84:85], s[48:49]
	s_or_b64 s[0:1], vcc, s[0:1]
	v_cmp_eq_f32_e64 s[84:85], v6, v16
	v_cndmask_b32_e64 v5, 0, 1, s[0:1]
	v_cmp_gt_f32_e32 vcc, v6, v16
	s_and_b64 s[0:1], s[84:85], s[50:51]
	s_or_b64 s[0:1], vcc, s[0:1]
	v_cmp_eq_f32_e64 s[84:85], v7, v16
	v_cndmask_b32_e64 v6, 0, 1, s[0:1]
	v_cmp_gt_f32_e32 vcc, v7, v16
	s_and_b64 s[0:1], s[84:85], s[52:53]
	v_add3_u32 v4, v12, v13, v4
	s_or_b64 s[0:1], vcc, s[0:1]
	s_waitcnt lgkmcnt(0)
	v_cmp_eq_f32_e64 s[84:85], v8, v16
	v_add3_u32 v4, v4, v5, v6
	v_cndmask_b32_e64 v5, 0, 1, s[0:1]
	v_cmp_gt_f32_e32 vcc, v8, v16
	s_and_b64 s[0:1], s[84:85], s[54:55]
	s_or_b64 s[0:1], vcc, s[0:1]
	v_cmp_eq_f32_e64 s[84:85], v9, v16
	v_cndmask_b32_e64 v6, 0, 1, s[0:1]
	v_cmp_gt_f32_e32 vcc, v9, v16
	s_and_b64 s[0:1], s[84:85], s[56:57]
	s_or_b64 s[0:1], vcc, s[0:1]
	v_cmp_eq_f32_e64 s[84:85], v10, v16
	v_add3_u32 v4, v4, v5, v6
	v_cndmask_b32_e64 v5, 0, 1, s[0:1]
	v_cmp_gt_f32_e32 vcc, v10, v16
	s_and_b64 s[0:1], s[84:85], s[58:59]
	s_or_b64 s[0:1], vcc, s[0:1]
	v_cndmask_b32_e64 v6, 0, 1, s[0:1]
	v_add3_u32 v12, v4, v5, v6
	ds_read_b128 v[4:7], v207 offset:96
	v_cmp_eq_f32_e64 s[84:85], v11, v16
	v_cmp_gt_f32_e32 vcc, v11, v16
	s_and_b64 s[0:1], s[84:85], s[60:61]
	s_or_b64 s[0:1], vcc, s[0:1]
	ds_read_b128 v[8:11], v207 offset:112
	s_waitcnt lgkmcnt(1)
	v_cmp_eq_f32_e64 s[84:85], v4, v16
	v_cndmask_b32_e64 v13, 0, 1, s[0:1]
	v_cmp_gt_f32_e32 vcc, v4, v16
	s_and_b64 s[0:1], s[84:85], s[62:63]
	s_or_b64 s[0:1], vcc, s[0:1]
	v_cmp_eq_f32_e64 s[84:85], v5, v16
	v_cndmask_b32_e64 v4, 0, 1, s[0:1]
	v_cmp_gt_f32_e32 vcc, v5, v16
	s_and_b64 s[0:1], s[84:85], s[64:65]
	s_or_b64 s[0:1], vcc, s[0:1]
	v_cmp_eq_f32_e64 s[84:85], v6, v16
	v_cndmask_b32_e64 v5, 0, 1, s[0:1]
	v_cmp_gt_f32_e32 vcc, v6, v16
	s_and_b64 s[0:1], s[84:85], s[66:67]
	s_or_b64 s[0:1], vcc, s[0:1]
	v_cmp_eq_f32_e64 s[84:85], v7, v16
	v_cndmask_b32_e64 v6, 0, 1, s[0:1]
	v_cmp_gt_f32_e32 vcc, v7, v16
	s_and_b64 s[0:1], s[84:85], s[68:69]
	s_or_b64 s[0:1], vcc, s[0:1]
	s_waitcnt lgkmcnt(0)
	v_cmp_eq_f32_e64 s[84:85], v8, v16
	v_cndmask_b32_e64 v7, 0, 1, s[0:1]
	v_cmp_gt_f32_e32 vcc, v8, v16
	s_and_b64 s[0:1], s[84:85], s[70:71]
	s_or_b64 s[0:1], vcc, s[0:1]
	v_cmp_eq_f32_e64 s[84:85], v9, v16
	v_cndmask_b32_e64 v8, 0, 1, s[0:1]
	v_cmp_gt_f32_e32 vcc, v9, v16
	s_and_b64 s[0:1], s[84:85], s[72:73]
	s_or_b64 s[0:1], vcc, s[0:1]
	v_cmp_eq_f32_e64 s[84:85], v10, v16
	v_cndmask_b32_e64 v9, 0, 1, s[0:1]
	v_cmp_gt_f32_e32 vcc, v10, v16
	s_and_b64 s[0:1], s[84:85], s[74:75]
	s_or_b64 s[0:1], vcc, s[0:1]
	v_cmp_gt_f32_e32 vcc, v11, v16
	v_cndmask_b32_e64 v10, 0, 1, s[0:1]
	s_waitcnt lgkmcnt(0)
	s_nop 0
	v_addc_co_u32_e32 v11, vcc, v12, v13, vcc
	v_add_u32_e32 v4, v11, v4
	v_add3_u32 v4, v4, v5, v6
	v_add3_u32 v4, v4, v7, v8
	v_add3_u32 v4, v4, v9, v10
	v_cmp_gt_u32_e64 s[84:85], 16, v4
	s_and_saveexec_b64 s[0:1], s[10:11]
	s_cbranch_execz .LBB0_611
	s_add_i32 vcc_lo, s76, 0
	v_mov_b32_e32 v4, vcc_lo
	v_mov_b64_e32 v[6:7], s[84:85]
	ds_write_b64 v4, v[6:7]
	s_branch .LBB0_611
.LBB0_614:
	v_mov_b32_e32 v180, v213
	v_mov_b32_e32 v214, v3
.LBB0_615:
	v_exp_f32_e32 v216, v172
	v_exp_f32_e32 v217, v176
	v_exp_f32_e32 v218, v169
	v_exp_f32_e32 v222, v174
	v_exp_f32_e32 v223, v178
	v_exp_f32_e32 v174, v170
	v_exp_f32_e32 v176, v177
	v_exp_f32_e32 v178, v173
	v_exp_f32_e32 v224, v179
	v_exp_f32_e32 v226, v175
	v_exp_f32_e32 v219, v171
	v_cvt_pk_bf16_f32 v170, v216, v218
	v_cvt_pk_bf16_f32 v171, v222, v174
	v_cvt_pk_bf16_f32 v172, v176, v178
	v_cvt_pk_bf16_f32 v173, v224, v226
	v_pk_add_f32 v[220:221], v[216:217], 0 op_sel_hi:[1,0]
	v_exp_f32_e32 v164, v164
	s_waitcnt lgkmcnt(14)
	v_mfma_f32_32x32x16_bf16 v[66:81], v[130:133], v[170:173], v[66:81]
	v_exp_f32_e32 v132, v162
	v_exp_f32_e32 v162, v145
	v_exp_f32_e32 v216, v163
	v_exp_f32_e32 v166, v166
	v_exp_f32_e32 v168, v168
	v_exp_f32_e32 v175, v135
	v_exp_f32_e32 v177, v17
	s_waitcnt lgkmcnt(12)
	v_mfma_f32_32x32x16_bf16 v[50:65], v[126:129], v[170:173], v[50:65]
	v_exp_f32_e32 v170, v165
	v_exp_f32_e32 v172, v167
	v_cvt_pk_bf16_f32 v126, v132, v162
	v_cvt_pk_bf16_f32 v127, v164, v216
	v_cvt_pk_bf16_f32 v128, v166, v170
	v_cvt_pk_bf16_f32 v129, v168, v172
	v_exp_f32_e32 v179, v16
	v_exp_f32_e32 v225, v137
	s_waitcnt lgkmcnt(10)
	v_mfma_f32_32x32x16_bf16 v[66:81], v[122:125], v[126:129], v[66:81]
	v_exp_f32_e32 v227, v134
	v_pk_add_f32 v[220:221], v[218:219], v[220:221]
	v_exp_f32_e32 v133, v140
	v_pk_add_f32 v[130:131], v[222:223], v[220:221]
	v_exp_f32_e32 v163, v138
	v_pk_add_f32 v[16:17], v[174:175], v[130:131]
	v_exp_f32_e32 v165, v139
	s_waitcnt lgkmcnt(8)
	v_mfma_f32_32x32x16_bf16 v[50:65], v[118:121], v[126:129], v[50:65]
	v_cvt_pk_bf16_f32 v118, v217, v219
	v_cvt_pk_bf16_f32 v119, v223, v175
	v_cvt_pk_bf16_f32 v120, v177, v179
	v_cvt_pk_bf16_f32 v121, v225, v227
	v_add_f32_e64 v16, v176, v16
	v_add_f32_e64 v17, v177, v17
	v_exp_f32_e32 v217, v136
	v_pk_add_f32 v[16:17], v[178:179], v[16:17]
	s_waitcnt lgkmcnt(6)
	v_mfma_f32_32x32x16_bf16 v[66:81], v[114:117], v[118:121], v[66:81]
	v_exp_f32_e32 v167, v142
	v_exp_f32_e32 v171, v141
	v_exp_f32_e32 v169, v144
	v_exp_f32_e32 v173, v143
	v_pk_add_f32 v[16:17], v[224:225], v[16:17]
	s_nop 0
	v_pk_add_f32 v[16:17], v[226:227], v[16:17]
	s_waitcnt lgkmcnt(4)
	v_mfma_f32_32x32x16_bf16 v[50:65], v[12:15], v[118:121], v[50:65]
	v_add_f32_e64 v16, v132, v16
	v_add_f32_e64 v17, v133, v17
	v_cvt_pk_bf16_f32 v12, v133, v163
	v_add_f32_e64 v16, v162, v16
	v_add_f32_e64 v17, v163, v17
	v_cvt_pk_bf16_f32 v13, v165, v217
	v_cvt_pk_bf16_f32 v14, v167, v171
	v_cvt_pk_bf16_f32 v15, v169, v173
	v_pk_add_f32 v[16:17], v[164:165], v[16:17]
	s_waitcnt lgkmcnt(2)
	v_mfma_f32_32x32x16_bf16 v[66:81], v[8:11], v[12:15], v[66:81]
	v_add_f32_e64 v8, v216, v16
	v_add_f32_e64 v9, v217, v17
	v_add_f32_e64 v8, v166, v8
	v_add_f32_e64 v9, v167, v9
	v_add_f32_e64 v8, v170, v8
	v_add_f32_e64 v9, v171, v9
	v_pk_add_f32 v[8:9], v[168:169], v[8:9]
	s_waitcnt lgkmcnt(0)
	v_mfma_f32_32x32x16_bf16 v[50:65], v[4:7], v[12:15], v[50:65]
	v_add_f32_e64 v8, v172, v8
	v_add_f32_e64 v9, v173, v9
	v_add_f32_e32 v8, v8, v9
	v_add_f32_e32 v114, v180, v8

.LBB0_617:
	s_andn2_b64 vcc, exec, s[0:1]
	s_cbranch_vccnz .LBB0_626
	s_sub_i32 s76, s2, s81
	s_cmp_lg_u32 s76, s78
	s_mov_b64 s[0:1], -1
	s_cbranch_scc0 .LBB0_622
	s_waitcnt lgkmcnt(0)
	v_lshrrev_b32_e32 v4, s76, v211
	v_and_b32_e32 v4, 1, v4
	v_add3_u32 v16, s3, v203, v202
	v_cmp_eq_u32_e32 vcc, 1, v4
	ds_read_b128 v[4:7], v16
	ds_read_b128 v[8:11], v16 offset:512
	ds_read_b128 v[12:15], v16 offset:2048
	ds_read_b128 v[82:85], v16 offset:2560
	ds_read_b128 v[86:89], v16 offset:4096
	ds_read_b128 v[90:93], v16 offset:4608
	ds_read_b128 v[94:97], v16 offset:6144
	ds_read_b128 v[98:101], v16 offset:6656
	v_cndmask_b32_e64 v114, v195, -v3, vcc
	v_mov_b32_e32 v115, v114
	v_mov_b32_e32 v116, v114
	v_mov_b32_e32 v117, v114
	v_mov_b32_e32 v118, v114
	v_mov_b32_e32 v119, v114
	v_mov_b32_e32 v120, v114
	v_mov_b32_e32 v121, v114
	v_mov_b32_e32 v122, v114
	v_mov_b32_e32 v123, v114
	v_mov_b32_e32 v124, v114
	v_mov_b32_e32 v125, v114
	v_mov_b32_e32 v126, v114
	v_mov_b32_e32 v127, v114
	v_mov_b32_e32 v128, v114
	v_mov_b32_e32 v129, v114
	s_waitcnt lgkmcnt(7)
	s_nop 0
	v_mfma_f32_32x32x16_bf16 v[130:145], v[4:7], v[158:161], v[114:129]
	v_add_u32_e32 v4, s3, v204
	v_add3_u32 v6, v4, v201, v205
	s_waitcnt lgkmcnt(6)
	v_mfma_f32_32x32x16_bf16 v[114:129], v[8:11], v[158:161], v[114:129]
	s_waitcnt lgkmcnt(5)
	v_mfma_f32_32x32x16_bf16 v[130:145], v[12:15], v[154:157], v[130:145]
	ds_read_b64_tr_b16 v[178:179], v6 offset:8192
	ds_read_b64_tr_b16 v[180:181], v6 offset:8704
	ds_read_b64_tr_b16 v[174:175], v6 offset:12288
	ds_read_b64_tr_b16 v[176:177], v6 offset:12800
	ds_read_b64_tr_b16 v[170:171], v6 offset:9216
	ds_read_b64_tr_b16 v[172:173], v6 offset:9728
	ds_read_b64_tr_b16 v[166:167], v6 offset:13312
	ds_read_b64_tr_b16 v[168:169], v6 offset:13824
	ds_read_b64_tr_b16 v[162:163], v6 offset:10240
	ds_read_b64_tr_b16 v[164:165], v6 offset:10752
	ds_read_b64_tr_b16 v[12:13], v6 offset:14336
	ds_read_b64_tr_b16 v[14:15], v6 offset:14848
	ds_read_b64_tr_b16 v[8:9], v6 offset:11264
	ds_read_b64_tr_b16 v[10:11], v6 offset:11776
	ds_read_b64_tr_b16 v[4:5], v6 offset:15360
	ds_read_b64_tr_b16 v[6:7], v6 offset:15872
	s_waitcnt lgkmcnt(14)
	v_mfma_f32_32x32x16_bf16 v[114:129], v[82:85], v[154:157], v[114:129]
	v_mfma_f32_32x32x16_bf16 v[130:145], v[86:89], v[150:153], v[130:145]
	v_mfma_f32_32x32x16_bf16 v[114:129], v[90:93], v[150:153], v[114:129]
	v_mfma_f32_32x32x16_bf16 v[130:145], v[94:97], v[146:149], v[130:145]
	v_mfma_f32_32x32x16_bf16 v[114:129], v[98:101], v[146:149], v[114:129]
	s_nop 10
	v_max_f32_e32 v16, v131, v131
	v_max_f32_e32 v17, v130, v130
	v_max_f32_e32 v16, v17, v16
	v_max3_f32 v17, v132, v133, v115
	v_max3_f32 v16, v16, v114, v116
	v_max3_f32 v16, v16, v117, v134
	v_max3_f32 v17, v17, v136, v137
	v_max3_f32 v16, v16, v135, v118
	v_max3_f32 v17, v17, v120, v121
	v_max3_f32 v16, v16, v119, v138
	v_max3_f32 v17, v17, v140, v141
	v_max3_f32 v16, v16, v139, v122
	v_max3_f32 v17, v17, v124, v125
	v_max3_f32 v16, v16, v123, v142
	v_max3_f32 v17, v17, v144, v145
	v_max3_f32 v16, v16, v143, v126
	v_max3_f32 v17, v17, v128, v129
	v_max3_f32 v16, v16, v127, v17
	v_mov_b32_e32 v17, v16
	s_nop 1
	v_permlane32_swap_b32_e32 v16, v17
	v_max_f32_e32 v17, v17, v17
	v_max_f32_e32 v16, v16, v16
	v_max_f32_e32 v17, v16, v17
	s_mov_b32 s0, 0x41000000
	v_cmp_lt_f32_e32 vcc, s0, v17
	s_cmp_eq_u64 vcc, 0
	s_cselect_b64 s[0:1], -1, 0
	s_xor_b64 s[86:87], s[84:85], -1
	s_and_b64 s[0:1], s[86:87], s[0:1]
	s_and_b64 vcc, exec, s[0:1]
	v_mov_b32_e32 v16, v213
	v_mov_b32_e32 v214, v3
	s_cbranch_vccnz .LBB0_621
	v_cndmask_b32_e64 v16, 0, v197, s[84:85]
	v_max_f32_e32 v17, v17, v17
	v_max_f32_e32 v16, v17, v16
	v_exp_f32_e64 v216, -v16
	v_add_f32_e32 v214, v3, v16
	v_pk_add_f32 v[130:131], v[130:131], v[16:17] op_sel_hi:[1,0] neg_lo:[0,1] neg_hi:[0,1]
	v_pk_add_f32 v[114:115], v[114:115], v[16:17] op_sel_hi:[1,0] neg_lo:[0,1] neg_hi:[0,1]
	v_pk_add_f32 v[132:133], v[132:133], v[16:17] op_sel_hi:[1,0] neg_lo:[0,1] neg_hi:[0,1]
	v_pk_add_f32 v[116:117], v[116:117], v[16:17] op_sel_hi:[1,0] neg_lo:[0,1] neg_hi:[0,1]
	v_pk_add_f32 v[134:135], v[134:135], v[16:17] op_sel_hi:[1,0] neg_lo:[0,1] neg_hi:[0,1]
	v_pk_add_f32 v[118:119], v[118:119], v[16:17] op_sel_hi:[1,0] neg_lo:[0,1] neg_hi:[0,1]
	v_pk_add_f32 v[136:137], v[136:137], v[16:17] op_sel_hi:[1,0] neg_lo:[0,1] neg_hi:[0,1]
	v_pk_add_f32 v[120:121], v[120:121], v[16:17] op_sel_hi:[1,0] neg_lo:[0,1] neg_hi:[0,1]
	v_pk_add_f32 v[138:139], v[138:139], v[16:17] op_sel_hi:[1,0] neg_lo:[0,1] neg_hi:[0,1]
	v_pk_add_f32 v[122:123], v[122:123], v[16:17] op_sel_hi:[1,0] neg_lo:[0,1] neg_hi:[0,1]
	v_pk_add_f32 v[140:141], v[140:141], v[16:17] op_sel_hi:[1,0] neg_lo:[0,1] neg_hi:[0,1]
	v_pk_add_f32 v[124:125], v[124:125], v[16:17] op_sel_hi:[1,0] neg_lo:[0,1] neg_hi:[0,1]
	v_pk_add_f32 v[142:143], v[142:143], v[16:17] op_sel_hi:[1,0] neg_lo:[0,1] neg_hi:[0,1]
	v_pk_add_f32 v[126:127], v[126:127], v[16:17] op_sel_hi:[1,0] neg_lo:[0,1] neg_hi:[0,1]
	v_pk_add_f32 v[144:145], v[144:145], v[16:17] op_sel_hi:[1,0] neg_lo:[0,1] neg_hi:[0,1]
	v_pk_add_f32 v[128:129], v[128:129], v[16:17] op_sel_hi:[1,0] neg_lo:[0,1] neg_hi:[0,1]
	v_pk_mul_f32 v[80:81], v[80:81], v[216:217] op_sel_hi:[1,0]
	v_pk_mul_f32 v[78:79], v[78:79], v[216:217] op_sel_hi:[1,0]
	v_pk_mul_f32 v[76:77], v[76:77], v[216:217] op_sel_hi:[1,0]
	v_pk_mul_f32 v[74:75], v[74:75], v[216:217] op_sel_hi:[1,0]
	v_pk_mul_f32 v[72:73], v[72:73], v[216:217] op_sel_hi:[1,0]
	v_pk_mul_f32 v[70:71], v[70:71], v[216:217] op_sel_hi:[1,0]
	v_pk_mul_f32 v[68:69], v[68:69], v[216:217] op_sel_hi:[1,0]
	v_pk_mul_f32 v[66:67], v[66:67], v[216:217] op_sel_hi:[1,0]
	v_pk_mul_f32 v[64:65], v[64:65], v[216:217] op_sel_hi:[1,0]
	v_pk_mul_f32 v[62:63], v[62:63], v[216:217] op_sel_hi:[1,0]
	v_pk_mul_f32 v[60:61], v[60:61], v[216:217] op_sel_hi:[1,0]
	v_pk_mul_f32 v[58:59], v[58:59], v[216:217] op_sel_hi:[1,0]
	v_pk_mul_f32 v[56:57], v[56:57], v[216:217] op_sel_hi:[1,0]
	v_pk_mul_f32 v[54:55], v[54:55], v[216:217] op_sel_hi:[1,0]
	v_pk_mul_f32 v[52:53], v[52:53], v[216:217] op_sel_hi:[1,0]
	v_pk_mul_f32 v[50:51], v[50:51], v[216:217] op_sel_hi:[1,0]
	v_mul_f32_e32 v16, v213, v216

.LBB0_625:
	v_exp_f32_e32 v108, v137
	v_exp_f32_e32 v109, v140
	v_exp_f32_e32 v110, v134
	v_exp_f32_e32 v111, v136
	v_exp_f32_e32 v112, v138
	v_exp_f32_e32 v134, v135
	v_exp_f32_e32 v136, v139
	v_exp_f32_e32 v138, v103
	v_exp_f32_e32 v140, v104
	v_exp_f32_e32 v142, v105
	v_cvt_pk_bf16_f32 v104, v108, v110
	v_cvt_pk_bf16_f32 v105, v112, v134
	v_cvt_pk_bf16_f32 v106, v136, v138
	v_cvt_pk_bf16_f32 v107, v140, v142
	v_pk_add_f32 v[96:97], v[108:109], 0 op_sel_hi:[1,0]
	v_exp_f32_e32 v113, v141
	s_waitcnt lgkmcnt(14)
	v_mfma_f32_32x32x16_bf16 v[66:81], v[130:133], v[104:107], v[66:81]
	v_add_f32_e64 v96, v110, v96
	v_add_f32_e64 v97, v111, v97
	v_exp_f32_e32 v132, v99
	v_exp_f32_e32 v98, v98
	v_exp_f32_e32 v108, v101
	v_exp_f32_e32 v100, v100
	v_exp_f32_e32 v102, v102
	v_exp_f32_e32 v110, v94
	s_waitcnt lgkmcnt(12)
	v_mfma_f32_32x32x16_bf16 v[50:65], v[126:129], v[104:107], v[50:65]
	v_exp_f32_e32 v104, v93
	v_exp_f32_e32 v106, v95
	v_pk_add_f32 v[130:131], v[112:113], v[96:97]
	v_cvt_pk_bf16_f32 v94, v132, v98
	v_cvt_pk_bf16_f32 v95, v108, v100
	v_cvt_pk_bf16_f32 v96, v102, v104
	v_cvt_pk_bf16_f32 v97, v106, v110
	v_exp_f32_e32 v135, v85
	v_exp_f32_e32 v137, v17
	s_waitcnt lgkmcnt(10)
	v_mfma_f32_32x32x16_bf16 v[66:81], v[122:125], v[94:97], v[66:81]
	v_exp_f32_e32 v139, v16
	v_exp_f32_e32 v141, v84
	v_exp_f32_e32 v143, v82
	v_pk_add_f32 v[16:17], v[134:135], v[130:131]
	v_exp_f32_e32 v133, v89
	v_exp_f32_e32 v99, v86
	v_exp_f32_e32 v101, v83
	s_waitcnt lgkmcnt(8)
	v_mfma_f32_32x32x16_bf16 v[50:65], v[118:121], v[94:97], v[50:65]
	v_cvt_pk_bf16_f32 v94, v109, v111
	v_cvt_pk_bf16_f32 v95, v113, v135
	v_cvt_pk_bf16_f32 v96, v137, v139
	v_cvt_pk_bf16_f32 v97, v141, v143
	v_exp_f32_e32 v109, v87
	v_exp_f32_e32 v103, v90
	v_exp_f32_e32 v105, v88
	s_waitcnt lgkmcnt(6)
	v_mfma_f32_32x32x16_bf16 v[66:81], v[114:117], v[94:97], v[66:81]
	v_exp_f32_e32 v107, v92
	v_exp_f32_e32 v111, v91
	v_pk_add_f32 v[16:17], v[136:137], v[16:17]
	v_mov_b32_e32 v214, v3
	v_pk_add_f32 v[16:17], v[138:139], v[16:17]
	s_nop 0
	v_pk_add_f32 v[16:17], v[140:141], v[16:17]
	s_waitcnt lgkmcnt(4)
	v_mfma_f32_32x32x16_bf16 v[50:65], v[12:15], v[94:97], v[50:65]
	v_add_f32_e64 v16, v142, v16
	v_add_f32_e64 v17, v143, v17
	v_cvt_pk_bf16_f32 v12, v133, v99
	v_cvt_pk_bf16_f32 v13, v109, v101
	v_cvt_pk_bf16_f32 v14, v103, v105
	v_cvt_pk_bf16_f32 v15, v107, v111
	v_pk_add_f32 v[16:17], v[132:133], v[16:17]
	s_waitcnt lgkmcnt(2)
	v_mfma_f32_32x32x16_bf16 v[66:81], v[8:11], v[12:15], v[66:81]
	v_add_f32_e64 v16, v98, v16
	v_add_f32_e64 v17, v99, v17
	v_add_f32_e64 v16, v108, v16
	v_add_f32_e64 v17, v109, v17
	v_add_f32_e64 v8, v100, v16
	v_add_f32_e64 v9, v101, v17
	s_waitcnt lgkmcnt(0)
	v_mfma_f32_32x32x16_bf16 v[50:65], v[4:7], v[12:15], v[50:65]
	v_add_f32_e64 v8, v102, v8
	v_add_f32_e64 v9, v103, v9
	v_add_f32_e64 v8, v104, v8
	v_add_f32_e64 v9, v105, v9
	v_pk_add_f32 v[8:9], v[106:107], v[8:9]
	v_pk_add_f32 v[8:9], v[110:111], v[8:9]
	v_add_f32_e32 v8, v8, v9
	v_add_f32_e32 v114, v213, v8

.LBB0_640:
	s_mov_b32 s30, s16
	s_mov_b32 s31, s16
	s_mov_b32 s17, s16
	s_mov_b32 s18, s16
	s_mov_b32 s19, s16
	s_mov_b32 s20, s16
	s_mov_b32 s21, s16
	s_mov_b32 s22, s16
	s_mov_b32 s23, s16
	s_mov_b32 s24, s16
	s_mov_b32 s25, s16
	s_mov_b32 s26, s16
	s_mov_b32 s27, s16
	s_mov_b32 s28, s16
	s_mov_b32 s29, s16
	v_mov_b64_e32 v[80:81], s[30:31]
	v_mov_b64_e32 v[78:79], s[28:29]
	v_mov_b64_e32 v[76:77], s[26:27]
	v_mov_b64_e32 v[74:75], s[24:25]
	v_mov_b64_e32 v[72:73], s[22:23]
	v_mov_b64_e32 v[70:71], s[20:21]
	v_mov_b64_e32 v[68:69], s[18:19]
	v_mov_b64_e32 v[66:67], s[16:17]
	v_mov_b64_e32 v[64:65], v[80:81]
	v_mov_b32_e32 v114, 0
	v_mov_b64_e32 v[62:63], v[78:79]
	v_mov_b64_e32 v[60:61], v[76:77]
	v_mov_b64_e32 v[58:59], v[74:75]
	v_mov_b64_e32 v[56:57], v[72:73]
	v_mov_b64_e32 v[54:55], v[70:71]
	v_mov_b64_e32 v[52:53], v[68:69]
	v_mov_b64_e32 v[50:51], v[66:67]
	s_branch .LBB0_559
